# stack + write-through (sc1) stores in GEMM epilogues to shorten release fences at grid barriers
# baseline (speedup 1.0000x reference)
.LBB0_198:
	s_and_saveexec_b64 s[4:5], s[18:19]
	s_cbranch_execz .LBB0_200
	global_load_dwordx4 v[146:149], v[138:139], off
	global_load_dwordx4 v[150:153], v[138:139], off offset:16
	v_ashrrev_i32_e32 v145, 31, v144
	v_or_b32_e32 v166, 16, v144
	v_or_b32_e32 v168, 32, v144
	v_or_b32_e32 v170, 48, v144
	v_lshlrev_b64 v[172:173], 6, v[144:145]
	v_ashrrev_i32_e32 v167, 31, v166
	v_ashrrev_i32_e32 v169, 31, v168
	s_movk_i32 s27, 0x2000
	v_ashrrev_i32_e32 v171, 31, v170
	v_lshl_add_u64 v[220:221], v[136:137], 0, v[172:173]
	v_lshlrev_b64 v[166:167], 6, v[166:167]
	v_lshlrev_b64 v[168:169], 6, v[168:169]
	s_mov_b64 s[28:29], 0x2000
	s_mov_b64 s[30:31], 0x2400
	v_lshlrev_b64 v[170:171], 6, v[170:171]
	v_lshl_add_u64 v[228:229], v[136:137], 0, v[166:167]
	v_lshl_add_u64 v[230:231], v[136:137], 0, v[168:169]
	v_add_co_u32_e32 v236, vcc, s27, v220
	v_lshl_add_u64 v[232:233], v[136:137], 0, v[170:171]
	v_lshl_add_u64 v[234:235], v[220:221], 0, s[28:29]
	v_addc_co_u32_e32 v237, vcc, 0, v221, vcc
	v_lshl_add_u64 v[238:239], v[220:221], 0, s[30:31]
	v_lshl_add_u64 v[240:241], v[220:221], 0, s[22:23]
	v_lshl_add_u64 v[242:243], v[220:221], 0, s[24:25]
	s_waitcnt vmcnt(0)
	v_pk_add_f32 v[168:169], v[128:129], v[148:149]
	v_pk_add_f32 v[166:167], v[126:127], v[146:147]
	v_pk_add_f32 v[172:173], v[124:125], v[152:153]
	v_pk_add_f32 v[170:171], v[122:123], v[150:151]
	v_pk_add_f32 v[176:177], v[120:121], v[148:149]
	v_pk_add_f32 v[174:175], v[118:119], v[146:147]
	v_pk_add_f32 v[180:181], v[112:113], v[152:153]
	v_pk_add_f32 v[178:179], v[110:111], v[150:151]
	v_pk_add_f32 v[184:185], v[104:105], v[148:149]
	v_pk_add_f32 v[182:183], v[102:103], v[146:147]
	v_pk_add_f32 v[188:189], v[96:97], v[152:153]
	v_pk_add_f32 v[186:187], v[94:95], v[150:151]
	v_pk_add_f32 v[192:193], v[88:89], v[148:149]
	v_pk_add_f32 v[190:191], v[86:87], v[146:147]
	v_pk_add_f32 v[196:197], v[80:81], v[152:153]
	v_pk_add_f32 v[194:195], v[78:79], v[150:151]
	v_pk_add_f32 v[202:203], v[64:65], v[148:149]
	v_pk_add_f32 v[200:201], v[62:63], v[146:147]
	v_pk_add_f32 v[206:207], v[60:61], v[152:153]
	v_pk_add_f32 v[204:205], v[58:59], v[150:151]
	v_pk_add_f32 v[210:211], v[48:49], v[148:149]
	v_pk_add_f32 v[208:209], v[46:47], v[146:147]
	v_pk_add_f32 v[214:215], v[32:33], v[152:153]
	v_pk_add_f32 v[212:213], v[30:31], v[150:151]
	v_pk_add_f32 v[218:219], v[24:25], v[148:149]
	v_pk_add_f32 v[216:217], v[22:23], v[146:147]
	v_pk_add_f32 v[226:227], v[16:17], v[152:153]
	v_pk_add_f32 v[224:225], v[14:15], v[150:151]
	v_pk_add_f32 v[148:149], v[8:9], v[148:149]
	v_pk_add_f32 v[146:147], v[6:7], v[146:147]
	v_pk_add_f32 v[152:153], v[4:5], v[152:153]
	v_pk_add_f32 v[150:151], v[2:3], v[150:151]
	global_store_dwordx4 v[220:221], v[166:169], off sc1
	global_store_dwordx4 v[220:221], v[170:173], off offset:16 sc1
	global_store_dwordx4 v[228:229], v[174:177], off sc1
	global_store_dwordx4 v[228:229], v[178:181], off offset:16 sc1
	global_store_dwordx4 v[230:231], v[182:185], off sc1
	global_store_dwordx4 v[230:231], v[186:189], off offset:16 sc1
	global_store_dwordx4 v[232:233], v[190:193], off sc1
	global_store_dwordx4 v[232:233], v[194:197], off offset:16 sc1
	global_store_dwordx4 v[236:237], v[200:203], off sc1
	global_store_dwordx4 v[234:235], v[204:207], off offset:16 sc1
	global_store_dwordx4 v[236:237], v[208:211], off offset:1024 sc1
	global_store_dwordx4 v[238:239], v[212:215], off offset:16 sc1
	global_store_dwordx4 v[236:237], v[216:219], off offset:2048 sc1
	global_store_dwordx4 v[240:241], v[224:227], off offset:16 sc1
	global_store_dwordx4 v[236:237], v[146:149], off offset:3072 sc1
	global_store_dwordx4 v[242:243], v[150:153], off offset:16 sc1

.LBB0_201:
	v_lshl_or_b32 v148, s49, 8, v157
	v_ashrrev_i32_e32 v149, 31, v148
	v_mov_b64_e32 v[146:147], s[12:13]
	v_mad_i64_i32 v[150:151], s[4:5], v144, s47, v[146:147]
	v_lshlrev_b64 v[148:149], 1, v[148:149]
	v_lshl_add_u64 v[150:151], v[150:151], 0, v[148:149]
	v_cvt_pk_bf16_f32 v126, v126, v127
	v_cvt_pk_bf16_f32 v127, v128, v129
	v_cvt_pk_bf16_f32 v128, v122, v123
	v_cvt_pk_bf16_f32 v129, v124, v125
	global_store_dwordx4 v[150:151], v[126:129], off sc1
	v_cvt_pk_bf16_f32 v114, v114, v115
	v_cvt_pk_bf16_f32 v115, v116, v117
	v_cvt_pk_bf16_f32 v116, v106, v107
	v_or_b32_e32 v106, 16, v144
	v_mad_i64_i32 v[106:107], s[4:5], v106, s47, v[146:147]
	v_cvt_pk_bf16_f32 v117, v108, v109
	global_store_dwordx4 v[150:151], v[114:117], off offset:256 sc1
	s_nop 1
	v_lshl_add_u64 v[114:115], v[106:107], 0, v[148:149]
	v_cvt_pk_bf16_f32 v106, v118, v119
	v_cvt_pk_bf16_f32 v107, v120, v121
	v_cvt_pk_bf16_f32 v108, v110, v111
	v_cvt_pk_bf16_f32 v109, v112, v113
	global_store_dwordx4 v[114:115], v[106:109], off sc1
	v_cvt_pk_bf16_f32 v98, v98, v99
	v_cvt_pk_bf16_f32 v99, v100, v101
	v_cvt_pk_bf16_f32 v100, v90, v91
	v_or_b32_e32 v90, 32, v144
	v_mad_i64_i32 v[90:91], s[4:5], v90, s47, v[146:147]
	v_cvt_pk_bf16_f32 v101, v92, v93
	global_store_dwordx4 v[114:115], v[98:101], off offset:256 sc1
	s_nop 1
	v_lshl_add_u64 v[98:99], v[90:91], 0, v[148:149]
	v_cvt_pk_bf16_f32 v90, v102, v103
	v_cvt_pk_bf16_f32 v91, v104, v105
	v_cvt_pk_bf16_f32 v92, v94, v95
	v_cvt_pk_bf16_f32 v93, v96, v97
	global_store_dwordx4 v[98:99], v[90:93], off sc1
	v_cvt_pk_bf16_f32 v82, v82, v83
	v_cvt_pk_bf16_f32 v83, v84, v85
	v_cvt_pk_bf16_f32 v84, v74, v75
	v_or_b32_e32 v74, 48, v144
	v_mad_i64_i32 v[74:75], s[4:5], v74, s47, v[146:147]
	v_cvt_pk_bf16_f32 v85, v76, v77
	global_store_dwordx4 v[98:99], v[82:85], off offset:256 sc1
	s_nop 1
	v_lshl_add_u64 v[82:83], v[74:75], 0, v[148:149]
	v_cvt_pk_bf16_f32 v74, v86, v87
	v_cvt_pk_bf16_f32 v75, v88, v89
	v_cvt_pk_bf16_f32 v76, v78, v79
	v_cvt_pk_bf16_f32 v77, v80, v81
	global_store_dwordx4 v[82:83], v[74:77], off sc1
	v_cvt_pk_bf16_f32 v70, v70, v71
	v_cvt_pk_bf16_f32 v71, v72, v73
	v_cvt_pk_bf16_f32 v72, v66, v67
	v_add_u32_e32 v66, 0x80, v144
	v_mad_i64_i32 v[66:67], s[4:5], v66, s47, v[146:147]
	v_lshl_add_u64 v[66:67], v[66:67], 0, v[148:149]
	v_cvt_pk_bf16_f32 v73, v68, v69
	global_store_dwordx4 v[82:83], v[70:73], off offset:256 sc1
	v_cvt_pk_bf16_f32 v62, v62, v63
	v_cvt_pk_bf16_f32 v63, v64, v65
	v_cvt_pk_bf16_f32 v64, v58, v59
	v_cvt_pk_bf16_f32 v65, v60, v61
	global_store_dwordx4 v[66:67], v[62:65], off sc1
	v_cvt_pk_bf16_f32 v42, v42, v43
	v_cvt_pk_bf16_f32 v43, v44, v45
	v_cvt_pk_bf16_f32 v44, v26, v27
	v_add_u32_e32 v26, 0x90, v144
	v_mad_i64_i32 v[26:27], s[4:5], v26, s47, v[146:147]
	v_cvt_pk_bf16_f32 v45, v28, v29
	global_store_dwordx4 v[66:67], v[42:45], off offset:256 sc1
	s_nop 1
	v_lshl_add_u64 v[42:43], v[26:27], 0, v[148:149]
	v_cvt_pk_bf16_f32 v26, v46, v47
	v_cvt_pk_bf16_f32 v27, v48, v49
	v_cvt_pk_bf16_f32 v28, v30, v31
	v_cvt_pk_bf16_f32 v29, v32, v33
	global_store_dwordx4 v[42:43], v[26:29], off sc1
	v_cvt_pk_bf16_f32 v18, v18, v19
	v_cvt_pk_bf16_f32 v19, v20, v21
	v_cvt_pk_bf16_f32 v20, v10, v11
	v_add_u32_e32 v10, 0xa0, v144
	v_mad_i64_i32 v[10:11], s[4:5], v10, s47, v[146:147]
	v_cvt_pk_bf16_f32 v21, v12, v13
	global_store_dwordx4 v[42:43], v[18:21], off offset:256 sc1
	s_nop 1
	v_lshl_add_u64 v[18:19], v[10:11], 0, v[148:149]
	v_cvt_pk_bf16_f32 v10, v22, v23
	v_cvt_pk_bf16_f32 v11, v24, v25
	v_cvt_pk_bf16_f32 v12, v14, v15
	v_cvt_pk_bf16_f32 v13, v16, v17
	global_store_dwordx4 v[18:19], v[10:13], off sc1
	s_nop 1
	v_cvt_pk_bf16_f32 v10, v54, v55
	v_cvt_pk_bf16_f32 v11, v56, v57
	v_cvt_pk_bf16_f32 v12, v50, v51
	v_cvt_pk_bf16_f32 v13, v52, v53
	global_store_dwordx4 v[18:19], v[10:13], off offset:256 sc1
	v_cvt_pk_bf16_f32 v6, v6, v7
	v_cvt_pk_bf16_f32 v7, v8, v9
	v_cvt_pk_bf16_f32 v8, v2, v3
	v_cvt_pk_bf16_f32 v9, v4, v5
	s_nop 1
	v_add_u32_e32 v10, 0xb0, v144
	v_mad_i64_i32 v[10:11], s[4:5], v10, s47, v[146:147]
	v_lshl_add_u64 v[10:11], v[10:11], 0, v[148:149]
	global_store_dwordx4 v[10:11], v[6:9], off sc1
	v_cvt_pk_bf16_f32 v2, v38, v39
	v_cvt_pk_bf16_f32 v3, v40, v41
	v_cvt_pk_bf16_f32 v4, v34, v35
	v_cvt_pk_bf16_f32 v5, v36, v37
	global_store_dwordx4 v[10:11], v[2:5], off offset:256 sc1
	s_and_b64 vcc, exec, s[2:3]
	s_mov_b64 s[2:3], -1
	s_cbranch_vccnz .LBB0_182

.LBB0_623:
	v_lshl_add_u32 v140, s6, 8, v149
	v_lshl_or_b32 v138, s28, 8, v151
	v_ashrrev_i32_e32 v141, 31, v140
	v_ashrrev_i32_e32 v139, 31, v138
	v_lshlrev_b64 v[142:143], 12, v[140:141]
	v_lshl_add_u64 v[142:143], s[12:13], 0, v[142:143]
	v_lshlrev_b64 v[144:145], 1, v[138:139]
	v_lshl_add_u64 v[138:139], v[142:143], 0, v[144:145]
	v_cvt_pk_bf16_f32 v126, v126, v127
	v_cvt_pk_bf16_f32 v127, v128, v129
	v_cvt_pk_bf16_f32 v128, v122, v123
	v_cvt_pk_bf16_f32 v129, v124, v125
	global_store_dwordx4 v[138:139], v[126:129], off sc1
	v_cvt_pk_bf16_f32 v114, v114, v115
	v_cvt_pk_bf16_f32 v115, v116, v117
	v_cvt_pk_bf16_f32 v116, v106, v107
	v_or_b32_e32 v106, 16, v140
	v_ashrrev_i32_e32 v107, 31, v106
	v_lshlrev_b64 v[106:107], 12, v[106:107]
	v_lshl_add_u64 v[106:107], s[12:13], 0, v[106:107]
	v_cvt_pk_bf16_f32 v117, v108, v109
	global_store_dwordx4 v[138:139], v[114:117], off offset:256 sc1
	s_nop 1
	v_lshl_add_u64 v[114:115], v[106:107], 0, v[144:145]
	v_cvt_pk_bf16_f32 v106, v118, v119
	v_cvt_pk_bf16_f32 v107, v120, v121
	v_cvt_pk_bf16_f32 v108, v110, v111
	v_cvt_pk_bf16_f32 v109, v112, v113
	global_store_dwordx4 v[114:115], v[106:109], off sc1
	v_cvt_pk_bf16_f32 v98, v98, v99
	v_cvt_pk_bf16_f32 v99, v100, v101
	v_cvt_pk_bf16_f32 v100, v90, v91
	v_or_b32_e32 v90, 32, v140
	v_ashrrev_i32_e32 v91, 31, v90
	v_lshlrev_b64 v[90:91], 12, v[90:91]
	v_lshl_add_u64 v[90:91], s[12:13], 0, v[90:91]
	v_cvt_pk_bf16_f32 v101, v92, v93
	global_store_dwordx4 v[114:115], v[98:101], off offset:256 sc1
	s_nop 1
	v_lshl_add_u64 v[98:99], v[90:91], 0, v[144:145]
	v_cvt_pk_bf16_f32 v90, v102, v103
	v_cvt_pk_bf16_f32 v91, v104, v105
	v_cvt_pk_bf16_f32 v92, v94, v95
	v_cvt_pk_bf16_f32 v93, v96, v97
	global_store_dwordx4 v[98:99], v[90:93], off sc1
	v_cvt_pk_bf16_f32 v82, v82, v83
	v_cvt_pk_bf16_f32 v83, v84, v85
	v_cvt_pk_bf16_f32 v84, v74, v75
	v_or_b32_e32 v74, 48, v140
	v_ashrrev_i32_e32 v75, 31, v74
	v_lshlrev_b64 v[74:75], 12, v[74:75]
	v_lshl_add_u64 v[74:75], s[12:13], 0, v[74:75]
	v_cvt_pk_bf16_f32 v85, v76, v77
	global_store_dwordx4 v[98:99], v[82:85], off offset:256 sc1
	s_nop 1
	v_lshl_add_u64 v[82:83], v[74:75], 0, v[144:145]
	v_cvt_pk_bf16_f32 v74, v86, v87
	v_cvt_pk_bf16_f32 v75, v88, v89
	v_cvt_pk_bf16_f32 v76, v78, v79
	v_cvt_pk_bf16_f32 v77, v80, v81
	global_store_dwordx4 v[82:83], v[74:77], off sc1
	v_cvt_pk_bf16_f32 v70, v70, v71
	v_cvt_pk_bf16_f32 v71, v72, v73
	v_cvt_pk_bf16_f32 v72, v66, v67
	v_cvt_pk_bf16_f32 v73, v68, v69
	global_store_dwordx4 v[82:83], v[70:73], off offset:256 sc1
	v_cvt_pk_bf16_f32 v62, v62, v63
	v_cvt_pk_bf16_f32 v63, v64, v65
	v_cvt_pk_bf16_f32 v64, v58, v59
	v_add_co_u32_e32 v58, vcc, s46, v138
	v_lshl_add_u64 v[66:67], v[138:139], 0, s[20:21]
	s_nop 0
	v_addc_co_u32_e32 v59, vcc, 0, v139, vcc
	v_cvt_pk_bf16_f32 v65, v60, v61
	global_store_dwordx4 v[58:59], v[62:65], off sc1
	v_cvt_pk_bf16_f32 v42, v42, v43
	v_cvt_pk_bf16_f32 v43, v44, v45
	v_cvt_pk_bf16_f32 v44, v30, v31
	v_cvt_pk_bf16_f32 v45, v32, v33
	global_store_dwordx4 v[66:67], v[42:45], off offset:256 sc1
	v_cvt_pk_bf16_f32 v30, v46, v47
	v_cvt_pk_bf16_f32 v31, v48, v49
	v_cvt_pk_bf16_f32 v32, v38, v39
	v_add_co_u32_e32 v38, vcc, s56, v138
	s_nop 0
	v_lshl_add_u64 v[42:43], v[138:139], 0, s[22:23]
	v_addc_co_u32_e32 v39, vcc, 0, v139, vcc
	v_cvt_pk_bf16_f32 v33, v40, v41
	global_store_dwordx4 v[38:39], v[30:33], off sc1
	v_cvt_pk_bf16_f32 v18, v18, v19
	v_cvt_pk_bf16_f32 v19, v20, v21
	v_cvt_pk_bf16_f32 v20, v10, v11
	v_cvt_pk_bf16_f32 v21, v12, v13
	global_store_dwordx4 v[42:43], v[18:21], off offset:256 sc1
	v_cvt_pk_bf16_f32 v10, v22, v23
	v_cvt_pk_bf16_f32 v11, v24, v25
	v_cvt_pk_bf16_f32 v12, v14, v15
	v_add_co_u32_e32 v14, vcc, s57, v138
	s_nop 0
	v_lshl_add_u64 v[18:19], v[138:139], 0, s[0:1]
	v_cvt_pk_bf16_f32 v13, v16, v17
	v_addc_co_u32_e32 v15, vcc, 0, v139, vcc
	global_store_dwordx4 v[14:15], v[10:13], off sc1
	s_nop 1
	v_cvt_pk_bf16_f32 v10, v54, v55
	v_cvt_pk_bf16_f32 v11, v56, v57
	v_cvt_pk_bf16_f32 v12, v50, v51
	v_cvt_pk_bf16_f32 v13, v52, v53
	global_store_dwordx4 v[18:19], v[10:13], off offset:256 sc1
	v_cvt_pk_bf16_f32 v6, v6, v7
	v_cvt_pk_bf16_f32 v7, v8, v9
	v_cvt_pk_bf16_f32 v8, v2, v3
	v_add_co_u32_e32 v2, vcc, s58, v138
	s_nop 0
	v_lshl_add_u64 v[10:11], v[138:139], 0, s[24:25]
	v_addc_co_u32_e32 v3, vcc, 0, v139, vcc
	v_cvt_pk_bf16_f32 v9, v4, v5
	global_store_dwordx4 v[2:3], v[6:9], off sc1
	v_cvt_pk_bf16_f32 v2, v34, v35
	v_cvt_pk_bf16_f32 v3, v36, v37
	v_cvt_pk_bf16_f32 v4, v26, v27
	v_cvt_pk_bf16_f32 v5, v28, v29
	global_store_dwordx4 v[10:11], v[2:5], off offset:256 sc1
	s_waitcnt vmcnt(0)
	s_and_saveexec_b64 s[28:29], s[2:3]
	s_cbranch_execz .LBB0_629
	s_mov_b64 s[36:37], exec
	v_mbcnt_lo_u32_b32 v2, s36, 0
	v_mbcnt_hi_u32_b32 v2, s37, v2
	v_cmp_eq_u32_e32 vcc, 0, v2
	s_and_saveexec_b64 s[34:35], vcc
	s_cbranch_execz .LBB0_626
	s_bcnt1_i32_b64 s7, s[36:37]
	v_mov_b32_e32 v3, s59
	v_mov_b32_e32 v4, s7
	s_waitcnt vmcnt(0)
	ds_add_rtn_u32 v3, v3, v4

.LBB0_933:
	v_mul_f32_e32 v2, 0xbfb8aa3b, v130
	v_exp_f32_e32 v2, v2
	v_mul_f32_e32 v126, v130, v126
	v_mul_f32_e32 v130, 0xbfb8aa3b, v133
	v_exp_f32_e32 v130, v130
	v_add_f32_e32 v2, 1.0, v2
	v_rcp_f32_e32 v2, v2
	v_lshl_add_u32 v134, s56, 8, v217
	v_ashrrev_i32_e32 v135, 31, v134
	v_lshlrev_b64 v[136:137], 12, v[134:135]
	v_mul_f32_e32 v2, v2, v126
	v_mul_f32_e32 v126, v131, v127
	v_mul_f32_e32 v127, 0xbfb8aa3b, v132
	v_exp_f32_e32 v127, v127
	v_mul_f32_e32 v135, 0xbfb8aa3b, v131
	v_add_f32_e32 v130, 1.0, v130
	v_mul_f32_e32 v131, 0xbfb8aa3b, v122
	v_add_f32_e32 v127, 1.0, v127
	v_rcp_f32_e32 v127, v127
	v_rcp_f32_e32 v130, v130
	v_exp_f32_e32 v131, v131
	v_mul_f32_e32 v128, v132, v128
	v_mul_f32_e32 v127, v127, v128
	v_mul_f32_e32 v128, v133, v129
	v_mul_f32_e32 v128, v130, v128
	v_add_f32_e32 v129, 1.0, v131
	v_mul_f32_e32 v130, 0xbfb8aa3b, v123
	v_rcp_f32_e32 v129, v129
	v_exp_f32_e32 v130, v130
	v_mul_f32_e32 v118, v122, v118
	v_exp_f32_e32 v135, v135
	v_mul_f32_e32 v122, v129, v118
	v_mul_f32_e32 v118, v123, v119
	v_add_f32_e32 v119, 1.0, v130
	v_mul_f32_e32 v123, 0xbfb8aa3b, v124
	v_rcp_f32_e32 v119, v119
	v_exp_f32_e32 v123, v123
	v_add_f32_e32 v135, 1.0, v135
	v_rcp_f32_e32 v135, v135
	v_mul_f32_e32 v130, v119, v118
	v_add_f32_e32 v118, 1.0, v123
	v_rcp_f32_e32 v118, v118
	v_mul_f32_e32 v120, v124, v120
	v_mul_f32_e32 v126, v135, v126
	v_mul_f32_e32 v129, 0xbfb8aa3b, v125
	v_mul_f32_e32 v123, v118, v120
	v_cvt_pk_bf16_f32 v120, v2, v126
	v_mul_f32_e32 v2, 0xbfb8aa3b, v114
	v_exp_f32_e32 v2, v2
	v_exp_f32_e32 v129, v129
	v_mul_f32_e32 v110, v114, v110
	v_mul_f32_e32 v114, 0xbfb8aa3b, v117
	v_add_f32_e32 v2, 1.0, v2
	v_rcp_f32_e32 v2, v2
	v_add_f32_e32 v119, 1.0, v129
	v_rcp_f32_e32 v119, v119
	v_lshl_or_b32 v4, s57, 7, v225
	v_mul_f32_e32 v2, v2, v110
	v_mul_f32_e32 v110, v115, v111
	v_mul_f32_e32 v111, 0xbfb8aa3b, v116
	v_exp_f32_e32 v111, v111
	v_exp_f32_e32 v114, v114
	v_ashrrev_i32_e32 v5, 31, v4
	v_mul_f32_e32 v118, v125, v121
	v_lshl_add_u64 v[136:137], s[16:17], 0, v[136:137]
	v_mul_f32_e32 v124, v119, v118
	v_lshlrev_b64 v[118:119], 1, v[4:5]
	v_lshl_add_u64 v[4:5], v[136:137], 0, v[118:119]
	v_cvt_pk_bf16_f32 v121, v127, v128
	v_cvt_pk_bf16_f32 v122, v122, v130
	v_add_f32_e32 v111, 1.0, v111
	v_cvt_pk_bf16_f32 v123, v123, v124
	global_store_dwordx4 v[4:5], v[120:123], off sc1
	v_rcp_f32_e32 v111, v111
	v_add_f32_e32 v114, 1.0, v114
	v_mul_f32_e32 v122, 0xbfb8aa3b, v115
	v_mul_f32_e32 v115, 0xbfb8aa3b, v106
	v_rcp_f32_e32 v114, v114
	v_exp_f32_e32 v115, v115
	v_mul_f32_e32 v112, v116, v112
	v_mul_f32_e32 v111, v111, v112
	v_mul_f32_e32 v112, v117, v113
	v_mul_f32_e32 v112, v114, v112
	v_add_f32_e32 v113, 1.0, v115
	v_mul_f32_e32 v114, 0xbfb8aa3b, v107
	v_rcp_f32_e32 v113, v113
	v_exp_f32_e32 v114, v114
	v_mul_f32_e32 v102, v106, v102
	v_mul_f32_e32 v106, 0xbfb8aa3b, v108
	v_mul_f32_e32 v113, v113, v102
	v_mul_f32_e32 v102, v107, v103
	v_add_f32_e32 v103, 1.0, v114
	v_rcp_f32_e32 v103, v103
	v_exp_f32_e32 v106, v106
	v_mul_f32_e32 v107, 0xbfb8aa3b, v109
	v_exp_f32_e32 v122, v122
	v_exp_f32_e32 v107, v107
	v_mul_f32_e32 v114, v103, v102
	v_add_f32_e32 v102, 1.0, v106
	v_add_f32_e32 v122, 1.0, v122
	v_rcp_f32_e32 v102, v102
	v_add_f32_e32 v103, 1.0, v107
	v_rcp_f32_e32 v122, v122
	v_rcp_f32_e32 v103, v103
	v_mul_f32_e32 v104, v108, v104
	v_mul_f32_e32 v108, v102, v104
	v_mul_f32_e32 v102, v109, v105
	v_mul_f32_e32 v110, v122, v110
	v_mul_f32_e32 v105, v103, v102
	v_cvt_pk_bf16_f32 v102, v2, v110
	v_mul_f32_e32 v2, 0xbfb8aa3b, v98
	v_exp_f32_e32 v2, v2
	v_mul_f32_e32 v94, v98, v94
	v_or_b32_e32 v120, 16, v134
	v_mul_f32_e32 v98, 0xbfb8aa3b, v101
	v_add_f32_e32 v2, 1.0, v2
	v_rcp_f32_e32 v2, v2
	v_ashrrev_i32_e32 v121, 31, v120
	v_exp_f32_e32 v98, v98
	v_lshlrev_b64 v[120:121], 12, v[120:121]
	v_mul_f32_e32 v2, v2, v94
	v_mul_f32_e32 v94, v99, v95
	v_mul_f32_e32 v95, 0xbfb8aa3b, v100
	v_exp_f32_e32 v95, v95
	v_lshl_add_u64 v[120:121], s[16:17], 0, v[120:121]
	v_lshl_add_u64 v[106:107], v[120:121], 0, v[118:119]
	v_cvt_pk_bf16_f32 v103, v111, v112
	v_cvt_pk_bf16_f32 v104, v113, v114
	v_add_f32_e32 v95, 1.0, v95
	v_cvt_pk_bf16_f32 v105, v108, v105
	global_store_dwordx4 v[106:107], v[102:105], off sc1
	v_rcp_f32_e32 v95, v95
	v_add_f32_e32 v98, 1.0, v98
	v_mul_f32_e32 v104, 0xbfb8aa3b, v99
	v_mul_f32_e32 v99, 0xbfb8aa3b, v90
	v_rcp_f32_e32 v98, v98
	v_exp_f32_e32 v99, v99
	v_mul_f32_e32 v96, v100, v96
	v_mul_f32_e32 v95, v95, v96
	v_mul_f32_e32 v96, v101, v97
	v_mul_f32_e32 v96, v98, v96
	v_add_f32_e32 v97, 1.0, v99
	v_mul_f32_e32 v98, 0xbfb8aa3b, v91
	v_rcp_f32_e32 v97, v97
	v_exp_f32_e32 v98, v98
	v_mul_f32_e32 v86, v90, v86
	v_mul_f32_e32 v90, 0xbfb8aa3b, v92
	v_mul_f32_e32 v97, v97, v86
	v_mul_f32_e32 v86, v91, v87
	v_add_f32_e32 v87, 1.0, v98
	v_rcp_f32_e32 v87, v87
	v_exp_f32_e32 v90, v90
	v_mul_f32_e32 v91, 0xbfb8aa3b, v93
	v_exp_f32_e32 v104, v104
	v_exp_f32_e32 v91, v91
	v_mul_f32_e32 v98, v87, v86
	v_add_f32_e32 v86, 1.0, v90
	v_add_f32_e32 v104, 1.0, v104
	v_rcp_f32_e32 v86, v86
	v_add_f32_e32 v87, 1.0, v91
	v_rcp_f32_e32 v104, v104
	v_rcp_f32_e32 v87, v87
	v_mul_f32_e32 v88, v92, v88
	v_mul_f32_e32 v92, v86, v88
	v_mul_f32_e32 v86, v93, v89
	v_mul_f32_e32 v94, v104, v94
	v_mul_f32_e32 v89, v87, v86
	v_cvt_pk_bf16_f32 v86, v2, v94
	v_mul_f32_e32 v2, 0xbfb8aa3b, v82
	v_exp_f32_e32 v2, v2
	v_mul_f32_e32 v78, v82, v78
	v_or_b32_e32 v102, 32, v134
	v_mul_f32_e32 v82, 0xbfb8aa3b, v85
	v_add_f32_e32 v2, 1.0, v2
	v_rcp_f32_e32 v2, v2
	v_ashrrev_i32_e32 v103, 31, v102
	v_exp_f32_e32 v82, v82
	v_lshlrev_b64 v[102:103], 12, v[102:103]
	v_mul_f32_e32 v2, v2, v78
	v_mul_f32_e32 v78, v83, v79
	v_mul_f32_e32 v79, 0xbfb8aa3b, v84
	v_exp_f32_e32 v79, v79
	v_lshl_add_u64 v[102:103], s[16:17], 0, v[102:103]
	v_lshl_add_u64 v[90:91], v[102:103], 0, v[118:119]
	v_cvt_pk_bf16_f32 v87, v95, v96
	v_cvt_pk_bf16_f32 v88, v97, v98
	v_add_f32_e32 v79, 1.0, v79
	v_cvt_pk_bf16_f32 v89, v92, v89
	global_store_dwordx4 v[90:91], v[86:89], off sc1
	v_rcp_f32_e32 v79, v79
	v_add_f32_e32 v82, 1.0, v82
	v_mul_f32_e32 v88, 0xbfb8aa3b, v83
	v_mul_f32_e32 v83, 0xbfb8aa3b, v74
	v_rcp_f32_e32 v82, v82
	v_exp_f32_e32 v83, v83
	v_mul_f32_e32 v80, v84, v80
	v_mul_f32_e32 v79, v79, v80
	v_mul_f32_e32 v80, v85, v81
	v_mul_f32_e32 v80, v82, v80
	v_add_f32_e32 v81, 1.0, v83
	v_mul_f32_e32 v82, 0xbfb8aa3b, v75
	v_rcp_f32_e32 v81, v81
	v_exp_f32_e32 v82, v82
	v_mul_f32_e32 v70, v74, v70
	v_mul_f32_e32 v74, 0xbfb8aa3b, v76
	v_mul_f32_e32 v81, v81, v70
	v_mul_f32_e32 v70, v75, v71
	v_add_f32_e32 v71, 1.0, v82
	v_rcp_f32_e32 v71, v71
	v_exp_f32_e32 v74, v74
	v_mul_f32_e32 v75, 0xbfb8aa3b, v77
	v_exp_f32_e32 v88, v88
	v_exp_f32_e32 v75, v75
	v_mul_f32_e32 v82, v71, v70
	v_add_f32_e32 v70, 1.0, v74
	v_add_f32_e32 v88, 1.0, v88
	v_rcp_f32_e32 v70, v70
	v_add_f32_e32 v71, 1.0, v75
	v_rcp_f32_e32 v88, v88
	v_rcp_f32_e32 v71, v71
	v_mul_f32_e32 v72, v76, v72
	v_mul_f32_e32 v76, v70, v72
	v_mul_f32_e32 v70, v77, v73
	v_mul_f32_e32 v78, v88, v78
	v_mul_f32_e32 v73, v71, v70
	v_cvt_pk_bf16_f32 v70, v2, v78
	v_mul_f32_e32 v2, 0xbfb8aa3b, v66
	v_exp_f32_e32 v2, v2
	v_mul_f32_e32 v62, v62, v66
	v_mul_f32_e32 v66, 0xbfb8aa3b, v69
	v_exp_f32_e32 v66, v66
	v_add_f32_e32 v2, 1.0, v2
	v_rcp_f32_e32 v2, v2
	v_cvt_pk_bf16_f32 v71, v79, v80
	v_cvt_pk_bf16_f32 v72, v81, v82
	v_cvt_pk_bf16_f32 v73, v76, v73
	v_mul_f32_e32 v76, 0xbfb8aa3b, v67
	v_mul_f32_e32 v2, v62, v2
	v_mul_f32_e32 v62, v63, v67
	v_mul_f32_e32 v63, 0xbfb8aa3b, v68
	v_exp_f32_e32 v63, v63
	v_add_f32_e32 v66, 1.0, v66
	v_mul_f32_e32 v67, 0xbfb8aa3b, v58
	v_rcp_f32_e32 v66, v66
	v_add_f32_e32 v63, 1.0, v63
	v_rcp_f32_e32 v63, v63
	v_exp_f32_e32 v67, v67
	v_mul_f32_e32 v64, v64, v68
	v_mul_f32_e32 v54, v54, v58
	v_mul_f32_e32 v63, v64, v63
	v_mul_f32_e32 v64, v65, v69
	v_mul_f32_e32 v64, v64, v66
	v_add_f32_e32 v65, 1.0, v67
	v_mul_f32_e32 v66, 0xbfb8aa3b, v59
	v_rcp_f32_e32 v65, v65
	v_exp_f32_e32 v66, v66
	v_or_b32_e32 v86, 48, v134
	v_ashrrev_i32_e32 v87, 31, v86
	v_mul_f32_e32 v58, v54, v65
	v_mul_f32_e32 v54, v55, v59
	v_add_f32_e32 v55, 1.0, v66
	v_mul_f32_e32 v59, 0xbfb8aa3b, v60
	v_rcp_f32_e32 v55, v55
	v_exp_f32_e32 v59, v59
	v_mul_f32_e32 v65, 0xbfb8aa3b, v61
	v_exp_f32_e32 v76, v76
	v_exp_f32_e32 v65, v65
	v_lshlrev_b64 v[86:87], 12, v[86:87]
	v_lshl_add_u64 v[86:87], s[16:17], 0, v[86:87]
	v_lshl_add_u64 v[74:75], v[86:87], 0, v[118:119]
	v_mul_f32_e32 v66, v54, v55
	v_add_f32_e32 v54, 1.0, v59
	global_store_dwordx4 v[74:75], v[70:73], off sc1
	v_rcp_f32_e32 v54, v54
	v_add_f32_e32 v55, 1.0, v65
	v_add_f32_e32 v70, 1.0, v76
	v_rcp_f32_e32 v70, v70
	v_rcp_f32_e32 v55, v55
	v_mul_f32_e32 v56, v56, v60
	v_mul_f32_e32 v59, v56, v54
	v_mul_f32_e32 v54, v57, v61
	v_mul_f32_e32 v62, v62, v70
	v_mul_f32_e32 v57, v54, v55
	v_cvt_pk_bf16_f32 v54, v2, v62
	v_mul_f32_e32 v2, 0xbfb8aa3b, v50
	v_exp_f32_e32 v2, v2
	v_mul_f32_e32 v46, v46, v50
	v_mul_f32_e32 v50, 0xbfb8aa3b, v53
	v_exp_f32_e32 v50, v50
	v_add_f32_e32 v2, 1.0, v2
	v_rcp_f32_e32 v2, v2
	v_mul_f32_e32 v60, 0xbfb8aa3b, v51
	v_add_f32_e32 v50, 1.0, v50
	v_rcp_f32_e32 v50, v50
	v_mul_f32_e32 v2, v46, v2
	v_mul_f32_e32 v46, v47, v51
	v_mul_f32_e32 v47, 0xbfb8aa3b, v52
	v_exp_f32_e32 v47, v47
	v_mul_f32_e32 v51, 0xbfb8aa3b, v42
	v_exp_f32_e32 v51, v51
	v_mul_f32_e32 v48, v48, v52
	v_add_f32_e32 v47, 1.0, v47
	v_rcp_f32_e32 v47, v47
	v_mul_f32_e32 v38, v38, v42
	v_exp_f32_e32 v60, v60
	v_cvt_pk_bf16_f32 v55, v63, v64
	v_mul_f32_e32 v47, v48, v47
	v_mul_f32_e32 v48, v49, v53
	v_mul_f32_e32 v48, v48, v50
	v_add_f32_e32 v49, 1.0, v51
	v_mul_f32_e32 v50, 0xbfb8aa3b, v43
	v_rcp_f32_e32 v49, v49
	v_exp_f32_e32 v50, v50
	v_cvt_pk_bf16_f32 v56, v58, v66
	v_add_co_u32_e32 v58, vcc, s52, v4
	v_mul_f32_e32 v42, v38, v49
	v_mul_f32_e32 v38, v39, v43
	v_add_f32_e32 v39, 1.0, v50
	v_mul_f32_e32 v43, 0xbfb8aa3b, v44
	v_rcp_f32_e32 v39, v39
	v_exp_f32_e32 v43, v43
	v_mul_f32_e32 v49, 0xbfb8aa3b, v45
	v_exp_f32_e32 v49, v49
	v_cvt_pk_bf16_f32 v57, v59, v57
	v_addc_co_u32_e32 v59, vcc, 0, v5, vcc
	v_mul_f32_e32 v50, v38, v39
	v_add_f32_e32 v38, 1.0, v43
	global_store_dwordx4 v[58:59], v[54:57], off sc1
	v_rcp_f32_e32 v38, v38
	v_add_f32_e32 v39, 1.0, v49
	v_add_f32_e32 v54, 1.0, v60
	v_rcp_f32_e32 v54, v54
	v_rcp_f32_e32 v39, v39
	v_mul_f32_e32 v40, v40, v44
	v_mul_f32_e32 v43, v40, v38
	v_mul_f32_e32 v38, v41, v45
	v_mul_f32_e32 v46, v46, v54
	v_mul_f32_e32 v41, v38, v39
	v_cvt_pk_bf16_f32 v38, v2, v46
	v_mul_f32_e32 v2, 0xbfb8aa3b, v30
	v_exp_f32_e32 v2, v2
	v_mul_f32_e32 v30, v30, v34
	v_mul_f32_e32 v44, 0xbfb8aa3b, v31
	v_mul_f32_e32 v34, 0xbfb8aa3b, v33
	v_add_f32_e32 v2, 1.0, v2
	v_rcp_f32_e32 v2, v2
	v_exp_f32_e32 v34, v34
	v_exp_f32_e32 v44, v44
	v_cvt_pk_bf16_f32 v39, v47, v48
	v_mul_f32_e32 v2, v2, v30
	v_mul_f32_e32 v30, v31, v35
	v_mul_f32_e32 v31, 0xbfb8aa3b, v32
	v_exp_f32_e32 v31, v31
	v_add_f32_e32 v34, 1.0, v34
	v_mul_f32_e32 v35, 0xbfb8aa3b, v22
	v_rcp_f32_e32 v34, v34
	v_add_f32_e32 v31, 1.0, v31
	v_rcp_f32_e32 v31, v31
	v_exp_f32_e32 v35, v35
	v_mul_f32_e32 v32, v32, v36
	v_mul_f32_e32 v22, v22, v26
	v_mul_f32_e32 v31, v31, v32
	v_mul_f32_e32 v32, v33, v37
	v_mul_f32_e32 v32, v34, v32
	v_add_f32_e32 v33, 1.0, v35
	v_mul_f32_e32 v34, 0xbfb8aa3b, v23
	v_rcp_f32_e32 v33, v33
	v_exp_f32_e32 v34, v34
	v_cvt_pk_bf16_f32 v40, v42, v50
	v_add_co_u32_e32 v42, vcc, s53, v4
	v_mul_f32_e32 v26, v33, v22
	v_mul_f32_e32 v22, v23, v27
	v_add_f32_e32 v23, 1.0, v34
	v_mul_f32_e32 v27, 0xbfb8aa3b, v24
	v_rcp_f32_e32 v23, v23
	v_exp_f32_e32 v27, v27
	v_mul_f32_e32 v33, 0xbfb8aa3b, v25
	v_exp_f32_e32 v33, v33
	v_cvt_pk_bf16_f32 v41, v43, v41
	v_addc_co_u32_e32 v43, vcc, 0, v5, vcc
	v_mul_f32_e32 v34, v23, v22
	v_add_f32_e32 v22, 1.0, v27
	global_store_dwordx4 v[42:43], v[38:41], off sc1
	v_rcp_f32_e32 v22, v22
	v_add_f32_e32 v23, 1.0, v33
	v_add_f32_e32 v38, 1.0, v44
	v_rcp_f32_e32 v38, v38
	v_rcp_f32_e32 v23, v23
	v_mul_f32_e32 v24, v24, v28
	v_mul_f32_e32 v27, v22, v24
	v_mul_f32_e32 v22, v25, v29
	v_mul_f32_e32 v30, v38, v30
	v_mul_f32_e32 v25, v23, v22
	v_cvt_pk_bf16_f32 v22, v2, v30
	v_mul_f32_e32 v2, 0xbfb8aa3b, v14
	v_exp_f32_e32 v2, v2
	v_mul_f32_e32 v14, v14, v18
	v_mul_f32_e32 v28, 0xbfb8aa3b, v15
	v_mul_f32_e32 v18, 0xbfb8aa3b, v17
	v_add_f32_e32 v2, 1.0, v2
	v_rcp_f32_e32 v2, v2
	v_exp_f32_e32 v18, v18
	v_exp_f32_e32 v28, v28
	v_cvt_pk_bf16_f32 v23, v31, v32
	v_mul_f32_e32 v2, v2, v14
	v_mul_f32_e32 v14, v15, v19
	v_mul_f32_e32 v15, 0xbfb8aa3b, v16
	v_exp_f32_e32 v15, v15
	v_add_f32_e32 v18, 1.0, v18
	v_mul_f32_e32 v19, 0xbfb8aa3b, v6
	v_rcp_f32_e32 v18, v18
	v_add_f32_e32 v15, 1.0, v15
	v_rcp_f32_e32 v15, v15
	v_exp_f32_e32 v19, v19
	v_mul_f32_e32 v16, v16, v20
	v_mul_f32_e32 v6, v6, v10
	v_mul_f32_e32 v15, v15, v16
	v_mul_f32_e32 v16, v17, v21
	v_mul_f32_e32 v16, v18, v16
	v_add_f32_e32 v17, 1.0, v19
	v_mul_f32_e32 v18, 0xbfb8aa3b, v7
	v_rcp_f32_e32 v17, v17
	v_exp_f32_e32 v18, v18
	v_cvt_pk_bf16_f32 v24, v26, v34
	v_add_co_u32_e32 v26, vcc, s54, v4
	v_mul_f32_e32 v10, v17, v6
	v_mul_f32_e32 v6, v7, v11
	v_add_f32_e32 v7, 1.0, v18
	v_mul_f32_e32 v11, 0xbfb8aa3b, v8
	v_rcp_f32_e32 v7, v7
	v_exp_f32_e32 v11, v11
	v_mul_f32_e32 v17, 0xbfb8aa3b, v9
	v_exp_f32_e32 v17, v17
	v_mul_f32_e32 v18, v7, v6
	v_add_f32_e32 v6, 1.0, v11
	v_cvt_pk_bf16_f32 v25, v27, v25
	v_addc_co_u32_e32 v27, vcc, 0, v5, vcc
	v_rcp_f32_e32 v6, v6
	v_add_f32_e32 v7, 1.0, v17
	global_store_dwordx4 v[26:27], v[22:25], off sc1
	v_rcp_f32_e32 v7, v7
	v_mul_f32_e32 v8, v8, v12
	v_add_f32_e32 v22, 1.0, v28
	v_rcp_f32_e32 v22, v22
	v_add_co_u32_e32 v4, vcc, 0xb0000, v4
	v_mul_f32_e32 v11, v6, v8
	v_mul_f32_e32 v6, v9, v13
	v_addc_co_u32_e32 v5, vcc, 0, v5, vcc
	v_mul_f32_e32 v9, v7, v6
	s_and_b64 vcc, exec, s[2:3]
	s_mov_b64 s[2:3], -1
	v_mul_f32_e32 v14, v22, v14
	v_cvt_pk_bf16_f32 v6, v2, v14
	v_cvt_pk_bf16_f32 v7, v15, v16
	v_cvt_pk_bf16_f32 v8, v10, v18
	v_cvt_pk_bf16_f32 v9, v11, v9
	global_store_dwordx4 v[4:5], v[6:9], off sc1
	s_cbranch_vccnz .LBB0_920
	s_andn2_b64 vcc, exec, s[14:15]
	s_cbranch_vccnz .LBB0_919
	s_barrier
	s_branch .LBB0_919

.LBB0_1010:
	v_lshl_add_u32 v134, s63, 8, v207
	v_lshl_or_b32 v132, s64, 8, v219
	v_ashrrev_i32_e32 v135, 31, v134
	v_ashrrev_i32_e32 v133, 31, v132
	v_lshlrev_b64 v[136:137], 12, v[134:135]
	v_lshl_add_u64 v[136:137], s[14:15], 0, v[136:137]
	v_lshlrev_b64 v[138:139], 1, v[132:133]
	v_lshl_add_u64 v[132:133], v[136:137], 0, v[138:139]
	v_cvt_pk_bf16_f32 v128, v128, v129
	v_cvt_pk_bf16_f32 v129, v130, v131
	v_cvt_pk_bf16_f32 v130, v124, v125
	v_cvt_pk_bf16_f32 v131, v126, v127
	global_store_dwordx4 v[132:133], v[128:131], off sc1
	v_cvt_pk_bf16_f32 v116, v116, v117
	v_cvt_pk_bf16_f32 v117, v118, v119
	v_cvt_pk_bf16_f32 v118, v108, v109
	v_or_b32_e32 v108, 16, v134
	v_ashrrev_i32_e32 v109, 31, v108
	v_lshlrev_b64 v[108:109], 12, v[108:109]
	v_lshl_add_u64 v[108:109], s[14:15], 0, v[108:109]
	v_cvt_pk_bf16_f32 v119, v110, v111
	global_store_dwordx4 v[132:133], v[116:119], off offset:256 sc1
	s_nop 1
	v_lshl_add_u64 v[116:117], v[108:109], 0, v[138:139]
	v_cvt_pk_bf16_f32 v108, v120, v121
	v_cvt_pk_bf16_f32 v109, v122, v123
	v_cvt_pk_bf16_f32 v110, v112, v113
	v_cvt_pk_bf16_f32 v111, v114, v115
	global_store_dwordx4 v[116:117], v[108:111], off sc1
	v_cvt_pk_bf16_f32 v100, v100, v101
	v_cvt_pk_bf16_f32 v101, v102, v103
	v_cvt_pk_bf16_f32 v102, v92, v93
	v_or_b32_e32 v92, 32, v134
	v_ashrrev_i32_e32 v93, 31, v92
	v_lshlrev_b64 v[92:93], 12, v[92:93]
	v_lshl_add_u64 v[92:93], s[14:15], 0, v[92:93]
	v_cvt_pk_bf16_f32 v103, v94, v95
	global_store_dwordx4 v[116:117], v[100:103], off offset:256 sc1
	s_nop 1
	v_lshl_add_u64 v[100:101], v[92:93], 0, v[138:139]
	v_cvt_pk_bf16_f32 v92, v104, v105
	v_cvt_pk_bf16_f32 v93, v106, v107
	v_cvt_pk_bf16_f32 v94, v96, v97
	v_cvt_pk_bf16_f32 v95, v98, v99
	global_store_dwordx4 v[100:101], v[92:95], off sc1
	v_cvt_pk_bf16_f32 v84, v84, v85
	v_cvt_pk_bf16_f32 v85, v86, v87
	v_cvt_pk_bf16_f32 v86, v76, v77
	v_or_b32_e32 v76, 48, v134
	v_ashrrev_i32_e32 v77, 31, v76
	v_lshlrev_b64 v[76:77], 12, v[76:77]
	v_lshl_add_u64 v[76:77], s[14:15], 0, v[76:77]
	v_cvt_pk_bf16_f32 v87, v78, v79
	global_store_dwordx4 v[100:101], v[84:87], off offset:256 sc1
	s_nop 1
	v_lshl_add_u64 v[84:85], v[76:77], 0, v[138:139]
	v_cvt_pk_bf16_f32 v76, v88, v89
	v_cvt_pk_bf16_f32 v77, v90, v91
	v_cvt_pk_bf16_f32 v78, v80, v81
	v_cvt_pk_bf16_f32 v79, v82, v83
	global_store_dwordx4 v[84:85], v[76:79], off sc1
	v_cvt_pk_bf16_f32 v72, v72, v73
	v_cvt_pk_bf16_f32 v73, v74, v75
	v_cvt_pk_bf16_f32 v74, v68, v69
	v_cvt_pk_bf16_f32 v75, v70, v71
	global_store_dwordx4 v[84:85], v[72:75], off offset:256 sc1
	v_cvt_pk_bf16_f32 v64, v64, v65
	v_cvt_pk_bf16_f32 v65, v66, v67
	v_cvt_pk_bf16_f32 v66, v60, v61
	v_add_co_u32_e32 v60, vcc, s53, v132
	v_lshl_add_u64 v[68:69], v[132:133], 0, s[22:23]
	s_nop 0
	v_addc_co_u32_e32 v61, vcc, 0, v133, vcc
	v_cvt_pk_bf16_f32 v67, v62, v63
	global_store_dwordx4 v[60:61], v[64:67], off sc1
	v_cvt_pk_bf16_f32 v56, v56, v57
	v_cvt_pk_bf16_f32 v57, v58, v59
	v_cvt_pk_bf16_f32 v58, v52, v53
	v_cvt_pk_bf16_f32 v59, v54, v55
	global_store_dwordx4 v[68:69], v[56:59], off offset:256 sc1
	v_cvt_pk_bf16_f32 v48, v48, v49
	v_cvt_pk_bf16_f32 v49, v50, v51
	v_cvt_pk_bf16_f32 v50, v44, v45
	v_add_co_u32_e32 v44, vcc, s59, v132
	v_lshl_add_u64 v[52:53], v[132:133], 0, s[24:25]
	s_nop 0
	v_addc_co_u32_e32 v45, vcc, 0, v133, vcc
	v_cvt_pk_bf16_f32 v51, v46, v47
	global_store_dwordx4 v[44:45], v[48:51], off sc1
	v_cvt_pk_bf16_f32 v40, v40, v41
	v_cvt_pk_bf16_f32 v41, v42, v43
	v_cvt_pk_bf16_f32 v42, v36, v37
	v_cvt_pk_bf16_f32 v43, v38, v39
	global_store_dwordx4 v[52:53], v[40:43], off offset:256 sc1
	v_cvt_pk_bf16_f32 v32, v32, v33
	v_cvt_pk_bf16_f32 v33, v34, v35
	v_cvt_pk_bf16_f32 v34, v28, v29
	v_add_co_u32_e32 v28, vcc, s60, v132
	v_lshl_add_u64 v[36:37], v[132:133], 0, s[26:27]
	s_nop 0
	v_addc_co_u32_e32 v29, vcc, 0, v133, vcc
	v_cvt_pk_bf16_f32 v35, v30, v31
	global_store_dwordx4 v[28:29], v[32:35], off sc1
	v_cvt_pk_bf16_f32 v24, v24, v25
	v_cvt_pk_bf16_f32 v25, v26, v27
	v_cvt_pk_bf16_f32 v26, v20, v21
	v_cvt_pk_bf16_f32 v27, v22, v23
	global_store_dwordx4 v[36:37], v[24:27], off offset:256 sc1
	v_cvt_pk_bf16_f32 v16, v16, v17
	v_cvt_pk_bf16_f32 v17, v18, v19
	v_cvt_pk_bf16_f32 v18, v12, v13
	v_add_co_u32_e32 v12, vcc, s61, v132
	v_lshl_add_u64 v[20:21], v[132:133], 0, s[28:29]
	s_nop 0
	v_addc_co_u32_e32 v13, vcc, 0, v133, vcc
	s_and_b64 vcc, exec, s[2:3]
	s_mov_b64 s[2:3], -1
	v_cvt_pk_bf16_f32 v19, v14, v15
	global_store_dwordx4 v[12:13], v[16:19], off sc1
	v_cvt_pk_bf16_f32 v8, v8, v9
	v_cvt_pk_bf16_f32 v9, v10, v11
	v_cvt_pk_bf16_f32 v10, v4, v5
	v_cvt_pk_bf16_f32 v11, v6, v7
	global_store_dwordx4 v[20:21], v[8:11], off offset:256 sc1
	s_cbranch_vccnz .LBB0_997
	s_andn2_b64 vcc, exec, s[12:13]
	s_cbranch_vccnz .LBB0_996
	s_barrier
	s_branch .LBB0_996

.LBB0_1153:
	v_lshl_or_b32 v144, s20, 8, v156
	v_ashrrev_i32_e32 v145, 31, v144
	v_lshl_add_u32 v134, s45, 8, v153
	v_mov_b64_e32 v[142:143], s[10:11]
	v_mad_i64_i32 v[146:147], s[22:23], v134, s43, v[142:143]
	v_lshlrev_b64 v[144:145], 1, v[144:145]
	v_lshl_add_u64 v[146:147], v[146:147], 0, v[144:145]
	v_cvt_pk_bf16_f32 v126, v126, v127
	v_cvt_pk_bf16_f32 v127, v128, v129
	v_cvt_pk_bf16_f32 v128, v122, v123
	v_cvt_pk_bf16_f32 v129, v124, v125
	global_store_dwordx4 v[146:147], v[126:129], off sc1
	v_cvt_pk_bf16_f32 v114, v114, v115
	v_cvt_pk_bf16_f32 v115, v116, v117
	v_cvt_pk_bf16_f32 v116, v106, v107
	v_or_b32_e32 v106, 16, v134
	v_mad_i64_i32 v[106:107], s[22:23], v106, s43, v[142:143]
	v_cvt_pk_bf16_f32 v117, v108, v109
	global_store_dwordx4 v[146:147], v[114:117], off offset:256 sc1
	s_and_b64 vcc, exec, s[2:3]
	s_mov_b64 s[2:3], -1
	v_lshl_add_u64 v[114:115], v[106:107], 0, v[144:145]
	v_cvt_pk_bf16_f32 v106, v118, v119
	v_cvt_pk_bf16_f32 v107, v120, v121
	v_cvt_pk_bf16_f32 v108, v110, v111
	v_cvt_pk_bf16_f32 v109, v112, v113
	global_store_dwordx4 v[114:115], v[106:109], off sc1
	v_cvt_pk_bf16_f32 v98, v98, v99
	v_cvt_pk_bf16_f32 v99, v100, v101
	v_cvt_pk_bf16_f32 v100, v90, v91
	v_or_b32_e32 v90, 32, v134
	v_mad_i64_i32 v[90:91], s[22:23], v90, s43, v[142:143]
	v_cvt_pk_bf16_f32 v101, v92, v93
	global_store_dwordx4 v[114:115], v[98:101], off offset:256 sc1
	s_nop 1
	v_lshl_add_u64 v[98:99], v[90:91], 0, v[144:145]
	v_cvt_pk_bf16_f32 v90, v102, v103
	v_cvt_pk_bf16_f32 v91, v104, v105
	v_cvt_pk_bf16_f32 v92, v94, v95
	v_cvt_pk_bf16_f32 v93, v96, v97
	global_store_dwordx4 v[98:99], v[90:93], off sc1
	v_cvt_pk_bf16_f32 v82, v82, v83
	v_cvt_pk_bf16_f32 v83, v84, v85
	v_cvt_pk_bf16_f32 v84, v74, v75
	v_or_b32_e32 v74, 48, v134
	v_mad_i64_i32 v[74:75], s[22:23], v74, s43, v[142:143]
	v_cvt_pk_bf16_f32 v85, v76, v77
	global_store_dwordx4 v[98:99], v[82:85], off offset:256 sc1
	s_nop 1
	v_lshl_add_u64 v[82:83], v[74:75], 0, v[144:145]
	v_cvt_pk_bf16_f32 v74, v86, v87
	v_cvt_pk_bf16_f32 v75, v88, v89
	v_cvt_pk_bf16_f32 v76, v78, v79
	v_cvt_pk_bf16_f32 v77, v80, v81
	global_store_dwordx4 v[82:83], v[74:77], off sc1
	v_cvt_pk_bf16_f32 v70, v70, v71
	v_cvt_pk_bf16_f32 v71, v72, v73
	v_cvt_pk_bf16_f32 v72, v66, v67
	v_add_u32_e32 v66, 0x80, v134
	v_mad_i64_i32 v[66:67], s[22:23], v66, s43, v[142:143]
	v_lshl_add_u64 v[66:67], v[66:67], 0, v[144:145]
	v_cvt_pk_bf16_f32 v73, v68, v69
	global_store_dwordx4 v[82:83], v[70:73], off offset:256 sc1
	v_cvt_pk_bf16_f32 v62, v62, v63
	v_cvt_pk_bf16_f32 v63, v64, v65
	v_cvt_pk_bf16_f32 v64, v58, v59
	v_cvt_pk_bf16_f32 v65, v60, v61
	global_store_dwordx4 v[66:67], v[62:65], off sc1
	v_cvt_pk_bf16_f32 v42, v42, v43
	v_cvt_pk_bf16_f32 v43, v44, v45
	v_cvt_pk_bf16_f32 v44, v26, v27
	v_add_u32_e32 v26, 0x90, v134
	v_mad_i64_i32 v[26:27], s[22:23], v26, s43, v[142:143]
	v_cvt_pk_bf16_f32 v45, v28, v29
	global_store_dwordx4 v[66:67], v[42:45], off offset:256 sc1
	s_nop 1
	v_lshl_add_u64 v[42:43], v[26:27], 0, v[144:145]
	v_cvt_pk_bf16_f32 v26, v46, v47
	v_cvt_pk_bf16_f32 v27, v48, v49
	v_cvt_pk_bf16_f32 v28, v30, v31
	v_cvt_pk_bf16_f32 v29, v32, v33
	global_store_dwordx4 v[42:43], v[26:29], off sc1
	v_cvt_pk_bf16_f32 v18, v18, v19
	v_cvt_pk_bf16_f32 v19, v20, v21
	v_cvt_pk_bf16_f32 v20, v10, v11
	v_add_u32_e32 v10, 0xa0, v134
	v_mad_i64_i32 v[10:11], s[22:23], v10, s43, v[142:143]
	v_cvt_pk_bf16_f32 v21, v12, v13
	global_store_dwordx4 v[42:43], v[18:21], off offset:256 sc1
	s_nop 1
	v_lshl_add_u64 v[18:19], v[10:11], 0, v[144:145]
	v_cvt_pk_bf16_f32 v10, v22, v23
	v_cvt_pk_bf16_f32 v11, v24, v25
	v_cvt_pk_bf16_f32 v12, v14, v15
	v_cvt_pk_bf16_f32 v13, v16, v17
	global_store_dwordx4 v[18:19], v[10:13], off sc1
	s_nop 1
	v_cvt_pk_bf16_f32 v10, v54, v55
	v_cvt_pk_bf16_f32 v11, v56, v57
	v_cvt_pk_bf16_f32 v12, v50, v51
	v_cvt_pk_bf16_f32 v13, v52, v53
	global_store_dwordx4 v[18:19], v[10:13], off offset:256 sc1
	v_cvt_pk_bf16_f32 v6, v6, v7
	v_cvt_pk_bf16_f32 v7, v8, v9
	v_cvt_pk_bf16_f32 v8, v2, v3
	v_cvt_pk_bf16_f32 v9, v4, v5
	s_nop 1
	v_add_u32_e32 v10, 0xb0, v134
	v_mad_i64_i32 v[10:11], s[22:23], v10, s43, v[142:143]
	v_lshl_add_u64 v[10:11], v[10:11], 0, v[144:145]
	global_store_dwordx4 v[10:11], v[6:9], off sc1
	v_cvt_pk_bf16_f32 v2, v38, v39
	v_cvt_pk_bf16_f32 v3, v40, v41
	v_cvt_pk_bf16_f32 v4, v34, v35
	v_cvt_pk_bf16_f32 v5, v36, v37
	global_store_dwordx4 v[10:11], v[2:5], off offset:256 sc1
	s_cbranch_vccnz .LBB0_1141
	s_andn2_b64 vcc, exec, s[0:1]
	s_cbranch_vccnz .LBB0_1140
	s_barrier
	s_branch .LBB0_1140

.LBB0_1300:
	v_mov_b64_e32 v[158:159], s[18:19]
	v_lshl_or_b32 v160, s33, 8, v155
	v_mad_i64_i32 v[158:159], s[6:7], v147, s52, v[158:159]
	v_cvt_pk_bf16_f32 v126, v126, v127
	v_cvt_pk_bf16_f32 v127, v128, v129
	v_cvt_pk_bf16_f32 v128, v122, v123
	v_or_b32_e32 v122, 16, v147
	v_cndmask_b32_e64 v123, 0, 1, s[0:1]
	v_ashrrev_i32_e32 v161, 31, v160
	v_cmp_ne_u32_e64 s[6:7], 1, v123
	v_lshlrev_b32_e32 v123, 8, v122
	v_lshl_add_u64 v[158:159], v[160:161], 1, v[158:159]
	v_cvt_pk_bf16_f32 v129, v124, v125
	s_andn2_b64 vcc, exec, s[0:1]
	v_and_b32_e32 v124, 0xfdf00, v123
	global_store_dwordx4 v[158:159], v[126:129], off sc1
	s_cbranch_vccnz .LBB0_1302
	v_mov_b32_e32 v125, v139
	v_lshl_add_u64 v[126:127], s[20:21], 0, v[124:125]
	v_lshl_add_u64 v[126:127], s[14:15], 2, v[126:127]
	v_mov_b32_e32 v157, v139
	v_lshl_add_u64 v[166:167], v[126:127], 0, v[156:157]
	global_load_dwordx4 v[126:129], v[166:167], off offset:-512
	global_load_dwordx4 v[162:165], v[166:167], off offset:-496
	global_load_dwordx4 v[172:175], v[166:167], off offset:-480
	global_load_dwordx4 v[176:179], v[166:167], off offset:-464
	v_mov_b32_e32 v123, v118
	v_mov_b32_e32 v125, v118
	v_mov_b32_e32 v149, v119
	v_mov_b32_e32 v151, v119
	v_mov_b32_e32 v153, v120
	v_mov_b32_e32 v157, v120
	v_mov_b32_e32 v171, v121
	v_mov_b32_e32 v180, v121
	v_mov_b32_e32 v182, v114
	v_mov_b32_e32 v184, v114
	v_mov_b32_e32 v183, v115
	v_mov_b32_e32 v185, v115
	v_mov_b32_e32 v186, v116
	v_mov_b32_e32 v187, v116
	v_mov_b32_e32 v188, v117
	v_mov_b32_e32 v189, v117
	v_permlane32_swap_b32_e32 v123, v125
	v_permlane32_swap_b32_e32 v149, v151
	v_permlane32_swap_b32_e32 v153, v157
	v_permlane32_swap_b32_e32 v171, v180
	v_permlane32_swap_b32_e32 v182, v184
	v_permlane32_swap_b32_e32 v183, v185
	v_permlane32_swap_b32_e32 v186, v187
	v_permlane32_swap_b32_e32 v188, v189
	v_cndmask_b32_e64 v167, v151, v149, s[2:3]
	v_cndmask_b32_e64 v166, v125, v123, s[2:3]
	v_cndmask_b32_e64 v181, v180, v171, s[2:3]
	v_cndmask_b32_e64 v180, v157, v153, s[2:3]
	v_cndmask_b32_e64 v183, v185, v183, s[2:3]
	v_cndmask_b32_e64 v182, v184, v182, s[2:3]
	v_cndmask_b32_e64 v185, v189, v188, s[2:3]
	v_cndmask_b32_e64 v184, v187, v186, s[2:3]
	s_waitcnt vmcnt(0)
	v_mov_b32_e32 v187, v128
	v_mov_b32_e32 v128, v127
	v_mov_b32_e32 v127, v164
	v_mov_b32_e32 v164, v163
	v_mov_b32_e32 v163, v174
	v_mov_b32_e32 v174, v173
	v_mov_b32_e32 v173, v178
	v_mov_b32_e32 v178, v177
	v_pk_mul_f32 v[128:129], v[128:129], v[166:167]
	v_pk_mul_f32 v[164:165], v[164:165], v[180:181]
	v_pk_mul_f32 v[166:167], v[174:175], v[182:183]
	v_pk_mul_f32 v[174:175], v[178:179], v[184:185]
	v_mov_b32_e32 v186, v126
	v_mov_b32_e32 v126, v162
	v_mov_b32_e32 v162, v172
	v_mov_b32_e32 v172, v176
	v_cndmask_b32_e64 v129, -v129, v129, s[2:3]
	v_cndmask_b32_e64 v128, -v128, v128, s[2:3]
	v_cndmask_b32_e64 v165, -v165, v165, s[2:3]
	v_cndmask_b32_e64 v164, -v164, v164, s[2:3]
	v_cndmask_b32_e64 v167, -v167, v167, s[2:3]
	v_cndmask_b32_e64 v166, -v166, v166, s[2:3]
	v_cndmask_b32_e64 v175, -v175, v175, s[2:3]
	v_cndmask_b32_e64 v174, -v174, v174, s[2:3]
	v_pk_fma_f32 v[118:119], v[118:119], v[186:187], v[128:129]
	v_pk_fma_f32 v[120:121], v[120:121], v[126:127], v[164:165]
	v_pk_fma_f32 v[114:115], v[114:115], v[162:163], v[166:167]
	v_pk_fma_f32 v[116:117], v[116:117], v[172:173], v[174:175]
.LBB0_1302:
	s_nop 0
	v_mov_b64_e32 v[126:127], s[18:19]
	v_cvt_pk_bf16_f32 v118, v118, v119
	v_cvt_pk_bf16_f32 v119, v120, v121
	v_cvt_pk_bf16_f32 v120, v114, v115
	v_or_b32_e32 v114, 32, v147
	v_mad_i64_i32 v[122:123], s[0:1], v122, s52, v[126:127]
	v_lshlrev_b32_e32 v115, 8, v114
	v_lshl_add_u64 v[122:123], v[160:161], 1, v[122:123]
	v_cvt_pk_bf16_f32 v121, v116, v117
	s_and_b64 vcc, exec, s[6:7]
	v_and_b32_e32 v116, 0xfef00, v115
	global_store_dwordx4 v[122:123], v[118:121], off sc1
	s_cbranch_vccnz .LBB0_1304
	v_mov_b32_e32 v117, v139
	v_lshl_add_u64 v[118:119], s[20:21], 0, v[116:117]
	v_lshl_add_u64 v[118:119], s[14:15], 2, v[118:119]
	v_mov_b32_e32 v157, v139
	v_lshl_add_u64 v[166:167], v[118:119], 0, v[156:157]
	global_load_dwordx4 v[118:121], v[166:167], off offset:-512
	global_load_dwordx4 v[126:129], v[166:167], off offset:-496
	global_load_dwordx4 v[162:165], v[166:167], off offset:-480
	global_load_dwordx4 v[172:175], v[166:167], off offset:-464
	v_mov_b32_e32 v115, v110
	v_mov_b32_e32 v117, v110
	v_mov_b32_e32 v125, v111
	v_mov_b32_e32 v149, v111
	v_mov_b32_e32 v151, v112
	v_mov_b32_e32 v153, v112
	v_mov_b32_e32 v157, v113
	v_mov_b32_e32 v171, v113
	v_mov_b32_e32 v178, v106
	v_mov_b32_e32 v180, v106
	v_mov_b32_e32 v179, v107
	v_mov_b32_e32 v181, v107
	v_mov_b32_e32 v182, v108
	v_mov_b32_e32 v183, v108
	v_mov_b32_e32 v184, v109
	v_mov_b32_e32 v185, v109
	v_permlane32_swap_b32_e32 v115, v117
	v_permlane32_swap_b32_e32 v125, v149
	v_permlane32_swap_b32_e32 v151, v153
	v_permlane32_swap_b32_e32 v157, v171
	v_permlane32_swap_b32_e32 v178, v180
	v_permlane32_swap_b32_e32 v179, v181
	v_permlane32_swap_b32_e32 v182, v183
	v_permlane32_swap_b32_e32 v184, v185
	v_cndmask_b32_e64 v167, v149, v125, s[2:3]
	v_cndmask_b32_e64 v166, v117, v115, s[2:3]
	v_cndmask_b32_e64 v177, v171, v157, s[2:3]
	v_cndmask_b32_e64 v176, v153, v151, s[2:3]
	v_cndmask_b32_e64 v179, v181, v179, s[2:3]
	v_cndmask_b32_e64 v178, v180, v178, s[2:3]
	v_cndmask_b32_e64 v181, v185, v184, s[2:3]
	v_cndmask_b32_e64 v180, v183, v182, s[2:3]
	s_waitcnt vmcnt(0)
	v_mov_b32_e32 v183, v120
	v_mov_b32_e32 v120, v119
	v_mov_b32_e32 v119, v128
	v_mov_b32_e32 v128, v127
	v_mov_b32_e32 v127, v164
	v_mov_b32_e32 v164, v163
	v_mov_b32_e32 v163, v174
	v_mov_b32_e32 v174, v173
	v_pk_mul_f32 v[120:121], v[120:121], v[166:167]
	v_pk_mul_f32 v[128:129], v[128:129], v[176:177]
	v_pk_mul_f32 v[164:165], v[164:165], v[178:179]
	v_pk_mul_f32 v[166:167], v[174:175], v[180:181]
	v_mov_b32_e32 v182, v118
	v_mov_b32_e32 v118, v126
	v_mov_b32_e32 v126, v162
	v_mov_b32_e32 v162, v172
	v_cndmask_b32_e64 v121, -v121, v121, s[2:3]
	v_cndmask_b32_e64 v120, -v120, v120, s[2:3]
	v_cndmask_b32_e64 v129, -v129, v129, s[2:3]
	v_cndmask_b32_e64 v128, -v128, v128, s[2:3]
	v_cndmask_b32_e64 v165, -v165, v165, s[2:3]
	v_cndmask_b32_e64 v164, -v164, v164, s[2:3]
	v_cndmask_b32_e64 v167, -v167, v167, s[2:3]
	v_cndmask_b32_e64 v166, -v166, v166, s[2:3]
	v_pk_fma_f32 v[110:111], v[110:111], v[182:183], v[120:121]
	v_pk_fma_f32 v[112:113], v[112:113], v[118:119], v[128:129]
	v_pk_fma_f32 v[106:107], v[106:107], v[126:127], v[164:165]
	v_pk_fma_f32 v[108:109], v[108:109], v[162:163], v[166:167]
.LBB0_1304:
	s_nop 0
	v_mov_b64_e32 v[118:119], s[18:19]
	v_cvt_pk_bf16_f32 v110, v110, v111
	v_cvt_pk_bf16_f32 v111, v112, v113
	v_cvt_pk_bf16_f32 v112, v106, v107
	v_or_b32_e32 v106, 48, v147
	v_mad_i64_i32 v[114:115], s[0:1], v114, s52, v[118:119]
	v_lshlrev_b32_e32 v107, 8, v106
	v_lshl_add_u64 v[114:115], v[160:161], 1, v[114:115]
	v_cvt_pk_bf16_f32 v113, v108, v109
	s_and_b64 vcc, exec, s[6:7]
	v_and_b32_e32 v108, 0xfff00, v107
	global_store_dwordx4 v[114:115], v[110:113], off sc1
	s_cbranch_vccnz .LBB0_1306
	v_mov_b32_e32 v109, v139
	v_lshl_add_u64 v[110:111], s[20:21], 0, v[108:109]
	v_lshl_add_u64 v[110:111], s[14:15], 2, v[110:111]
	v_mov_b32_e32 v157, v139
	v_lshl_add_u64 v[162:163], v[110:111], 0, v[156:157]
	global_load_dwordx4 v[110:113], v[162:163], off offset:-512
	global_load_dwordx4 v[118:121], v[162:163], off offset:-496
	global_load_dwordx4 v[126:129], v[162:163], off offset:-480
	s_nop 0
	global_load_dwordx4 v[162:165], v[162:163], off offset:-464
	v_mov_b32_e32 v107, v102
	v_mov_b32_e32 v109, v102
	v_mov_b32_e32 v117, v103
	v_mov_b32_e32 v125, v103
	v_mov_b32_e32 v149, v104
	v_mov_b32_e32 v151, v104
	v_mov_b32_e32 v153, v105
	v_mov_b32_e32 v157, v105
	v_mov_b32_e32 v171, v98
	v_mov_b32_e32 v174, v98
	v_mov_b32_e32 v175, v99
	v_mov_b32_e32 v176, v99
	v_mov_b32_e32 v178, v100
	v_mov_b32_e32 v179, v100
	v_mov_b32_e32 v177, v101
	v_mov_b32_e32 v180, v101
	v_permlane32_swap_b32_e32 v107, v109
	v_permlane32_swap_b32_e32 v117, v125
	v_permlane32_swap_b32_e32 v149, v151
	v_permlane32_swap_b32_e32 v153, v157
	v_permlane32_swap_b32_e32 v171, v174
	v_permlane32_swap_b32_e32 v175, v176
	v_permlane32_swap_b32_e32 v178, v179
	v_permlane32_swap_b32_e32 v177, v180
	v_cndmask_b32_e64 v167, v125, v117, s[2:3]
	v_cndmask_b32_e64 v166, v109, v107, s[2:3]
	v_cndmask_b32_e64 v173, v157, v153, s[2:3]
	v_cndmask_b32_e64 v172, v151, v149, s[2:3]
	v_cndmask_b32_e64 v175, v176, v175, s[2:3]
	v_cndmask_b32_e64 v174, v174, v171, s[2:3]
	v_cndmask_b32_e64 v177, v180, v177, s[2:3]
	v_cndmask_b32_e64 v176, v179, v178, s[2:3]
	s_waitcnt vmcnt(0)
	v_mov_b32_e32 v179, v112
	v_mov_b32_e32 v112, v111
	v_mov_b32_e32 v111, v120
	v_mov_b32_e32 v120, v119
	v_mov_b32_e32 v119, v128
	v_mov_b32_e32 v128, v127
	v_mov_b32_e32 v127, v164
	v_mov_b32_e32 v164, v163
	v_mov_b32_e32 v178, v110
	v_mov_b32_e32 v110, v118
	v_mov_b32_e32 v118, v126
	v_mov_b32_e32 v126, v162
	v_pk_mul_f32 v[112:113], v[112:113], v[166:167]
	v_pk_mul_f32 v[120:121], v[120:121], v[172:173]
	v_pk_mul_f32 v[128:129], v[128:129], v[174:175]
	v_pk_mul_f32 v[162:163], v[164:165], v[176:177]
	v_cndmask_b32_e64 v113, -v113, v113, s[2:3]
	v_cndmask_b32_e64 v112, -v112, v112, s[2:3]
	v_cndmask_b32_e64 v121, -v121, v121, s[2:3]
	v_cndmask_b32_e64 v120, -v120, v120, s[2:3]
	v_cndmask_b32_e64 v129, -v129, v129, s[2:3]
	v_cndmask_b32_e64 v128, -v128, v128, s[2:3]
	v_cndmask_b32_e64 v163, -v163, v163, s[2:3]
	v_cndmask_b32_e64 v162, -v162, v162, s[2:3]
	v_pk_fma_f32 v[102:103], v[102:103], v[178:179], v[112:113]
	v_pk_fma_f32 v[104:105], v[104:105], v[110:111], v[120:121]
	v_pk_fma_f32 v[98:99], v[98:99], v[118:119], v[128:129]
	v_pk_fma_f32 v[100:101], v[100:101], v[126:127], v[162:163]
.LBB0_1306:
	s_nop 0
	v_mov_b64_e32 v[110:111], s[18:19]
	v_cvt_pk_bf16_f32 v102, v102, v103
	v_cvt_pk_bf16_f32 v103, v104, v105
	v_cvt_pk_bf16_f32 v104, v98, v99
	v_add_u32_e32 v98, 0x80, v147
	v_mad_i64_i32 v[106:107], s[0:1], v106, s52, v[110:111]
	v_lshlrev_b32_e32 v99, 8, v98
	v_lshl_add_u64 v[106:107], v[160:161], 1, v[106:107]
	v_cvt_pk_bf16_f32 v105, v100, v101
	s_and_b64 vcc, exec, s[6:7]
	v_and_b32_e32 v100, 0xfcf00, v99
	global_store_dwordx4 v[106:107], v[102:105], off sc1
	s_cbranch_vccnz .LBB0_1308
	v_mov_b32_e32 v101, v139
	v_lshl_add_u64 v[102:103], s[20:21], 0, v[100:101]
	v_lshl_add_u64 v[102:103], s[14:15], 2, v[102:103]
	v_mov_b32_e32 v157, v139
	v_lshl_add_u64 v[126:127], v[102:103], 0, v[156:157]
	global_load_dwordx4 v[102:105], v[126:127], off offset:-512
	global_load_dwordx4 v[110:113], v[126:127], off offset:-496
	global_load_dwordx4 v[118:121], v[126:127], off offset:-480
	s_nop 0
	global_load_dwordx4 v[126:129], v[126:127], off offset:-464
	v_mov_b32_e32 v99, v94
	v_mov_b32_e32 v101, v94
	v_mov_b32_e32 v109, v95
	v_mov_b32_e32 v117, v95
	v_mov_b32_e32 v125, v96
	v_mov_b32_e32 v149, v96
	v_mov_b32_e32 v151, v97
	v_mov_b32_e32 v153, v97
	v_mov_b32_e32 v157, v90
	v_mov_b32_e32 v166, v90
	v_mov_b32_e32 v167, v91
	v_mov_b32_e32 v171, v91
	v_mov_b32_e32 v172, v92
	v_mov_b32_e32 v174, v92
	v_mov_b32_e32 v173, v93
	v_mov_b32_e32 v175, v93
	v_permlane32_swap_b32_e32 v99, v101
	v_permlane32_swap_b32_e32 v109, v117
	v_permlane32_swap_b32_e32 v125, v149
	v_permlane32_swap_b32_e32 v151, v153
	v_permlane32_swap_b32_e32 v157, v166
	v_permlane32_swap_b32_e32 v167, v171
	v_permlane32_swap_b32_e32 v172, v174
	v_permlane32_swap_b32_e32 v173, v175
	v_cndmask_b32_e64 v163, v117, v109, s[2:3]
	v_cndmask_b32_e64 v162, v101, v99, s[2:3]
	v_cndmask_b32_e64 v165, v153, v151, s[2:3]
	v_cndmask_b32_e64 v164, v149, v125, s[2:3]
	v_cndmask_b32_e64 v167, v171, v167, s[2:3]
	v_cndmask_b32_e64 v166, v166, v157, s[2:3]
	v_cndmask_b32_e64 v173, v175, v173, s[2:3]
	v_cndmask_b32_e64 v172, v174, v172, s[2:3]
	s_waitcnt vmcnt(0)
	v_mov_b32_e32 v175, v104
	v_mov_b32_e32 v104, v103
	v_mov_b32_e32 v103, v112
	v_mov_b32_e32 v112, v111
	v_mov_b32_e32 v111, v120
	v_mov_b32_e32 v120, v119
	v_mov_b32_e32 v119, v128
	v_mov_b32_e32 v128, v127
	v_mov_b32_e32 v174, v102
	v_mov_b32_e32 v102, v110
	v_mov_b32_e32 v110, v118
	v_mov_b32_e32 v118, v126
	v_pk_mul_f32 v[104:105], v[104:105], v[162:163]
	v_pk_mul_f32 v[112:113], v[112:113], v[164:165]
	v_pk_mul_f32 v[120:121], v[120:121], v[166:167]
	v_pk_mul_f32 v[126:127], v[128:129], v[172:173]
	v_cndmask_b32_e64 v105, -v105, v105, s[2:3]
	v_cndmask_b32_e64 v104, -v104, v104, s[2:3]
	v_cndmask_b32_e64 v113, -v113, v113, s[2:3]
	v_cndmask_b32_e64 v112, -v112, v112, s[2:3]
	v_cndmask_b32_e64 v121, -v121, v121, s[2:3]
	v_cndmask_b32_e64 v120, -v120, v120, s[2:3]
	v_cndmask_b32_e64 v127, -v127, v127, s[2:3]
	v_cndmask_b32_e64 v126, -v126, v126, s[2:3]
	v_pk_fma_f32 v[94:95], v[94:95], v[174:175], v[104:105]
	v_pk_fma_f32 v[96:97], v[96:97], v[102:103], v[112:113]
	v_pk_fma_f32 v[90:91], v[90:91], v[110:111], v[120:121]
	v_pk_fma_f32 v[92:93], v[92:93], v[118:119], v[126:127]
.LBB0_1308:
	s_nop 0
	v_mov_b64_e32 v[102:103], s[18:19]
	v_cvt_pk_bf16_f32 v94, v94, v95
	v_cvt_pk_bf16_f32 v95, v96, v97
	v_cvt_pk_bf16_f32 v96, v90, v91
	v_add_u32_e32 v90, 0x90, v147
	v_mad_i64_i32 v[98:99], s[0:1], v98, s52, v[102:103]
	v_lshlrev_b32_e32 v91, 8, v90
	v_lshl_add_u64 v[98:99], v[160:161], 1, v[98:99]
	v_cvt_pk_bf16_f32 v97, v92, v93
	s_and_b64 vcc, exec, s[6:7]
	v_and_b32_e32 v92, 0xfdf00, v91
	global_store_dwordx4 v[98:99], v[94:97], off sc1
	s_cbranch_vccnz .LBB0_1310
	v_mov_b32_e32 v93, v139
	v_lshl_add_u64 v[94:95], s[20:21], 0, v[92:93]
	v_lshl_add_u64 v[94:95], s[14:15], 2, v[94:95]
	v_mov_b32_e32 v157, v139
	v_lshl_add_u64 v[118:119], v[94:95], 0, v[156:157]
	global_load_dwordx4 v[94:97], v[118:119], off offset:-512
	global_load_dwordx4 v[102:105], v[118:119], off offset:-496
	global_load_dwordx4 v[110:113], v[118:119], off offset:-480
	s_nop 0
	global_load_dwordx4 v[118:121], v[118:119], off offset:-464
	v_mov_b32_e32 v91, v86
	v_mov_b32_e32 v93, v86
	v_mov_b32_e32 v101, v87
	v_mov_b32_e32 v109, v87
	v_mov_b32_e32 v117, v88
	v_mov_b32_e32 v125, v88
	v_mov_b32_e32 v128, v89
	v_mov_b32_e32 v129, v89
	v_mov_b32_e32 v149, v82
	v_mov_b32_e32 v151, v82
	v_mov_b32_e32 v153, v83
	v_mov_b32_e32 v157, v83
	v_mov_b32_e32 v164, v84
	v_mov_b32_e32 v166, v84
	v_mov_b32_e32 v165, v85
	v_mov_b32_e32 v167, v85
	v_permlane32_swap_b32_e32 v91, v93
	v_permlane32_swap_b32_e32 v101, v109
	v_permlane32_swap_b32_e32 v117, v125
	v_permlane32_swap_b32_e32 v128, v129
	v_permlane32_swap_b32_e32 v149, v151
	v_permlane32_swap_b32_e32 v153, v157
	v_permlane32_swap_b32_e32 v164, v166
	v_permlane32_swap_b32_e32 v165, v167
	v_cndmask_b32_e64 v127, v109, v101, s[2:3]
	v_cndmask_b32_e64 v126, v93, v91, s[2:3]
	v_cndmask_b32_e64 v129, v129, v128, s[2:3]
	v_cndmask_b32_e64 v128, v125, v117, s[2:3]
	v_cndmask_b32_e64 v163, v157, v153, s[2:3]
	v_cndmask_b32_e64 v162, v151, v149, s[2:3]
	v_cndmask_b32_e64 v165, v167, v165, s[2:3]
	v_cndmask_b32_e64 v164, v166, v164, s[2:3]
	s_waitcnt vmcnt(0)
	v_mov_b32_e32 v167, v96
	v_mov_b32_e32 v96, v95
	v_mov_b32_e32 v95, v104
	v_mov_b32_e32 v104, v103
	v_mov_b32_e32 v103, v112
	v_mov_b32_e32 v112, v111
	v_mov_b32_e32 v111, v120
	v_mov_b32_e32 v120, v119
	v_mov_b32_e32 v166, v94
	v_mov_b32_e32 v94, v102
	v_mov_b32_e32 v102, v110
	v_mov_b32_e32 v110, v118
	v_pk_mul_f32 v[96:97], v[96:97], v[126:127]
	v_pk_mul_f32 v[104:105], v[104:105], v[128:129]
	v_pk_mul_f32 v[112:113], v[112:113], v[162:163]
	v_pk_mul_f32 v[118:119], v[120:121], v[164:165]
	v_cndmask_b32_e64 v97, -v97, v97, s[2:3]
	v_cndmask_b32_e64 v96, -v96, v96, s[2:3]
	v_cndmask_b32_e64 v105, -v105, v105, s[2:3]
	v_cndmask_b32_e64 v104, -v104, v104, s[2:3]
	v_cndmask_b32_e64 v113, -v113, v113, s[2:3]
	v_cndmask_b32_e64 v112, -v112, v112, s[2:3]
	v_cndmask_b32_e64 v119, -v119, v119, s[2:3]
	v_cndmask_b32_e64 v118, -v118, v118, s[2:3]
	v_pk_fma_f32 v[86:87], v[86:87], v[166:167], v[96:97]
	v_pk_fma_f32 v[88:89], v[88:89], v[94:95], v[104:105]
	v_pk_fma_f32 v[82:83], v[82:83], v[102:103], v[112:113]
	v_pk_fma_f32 v[84:85], v[84:85], v[110:111], v[118:119]
.LBB0_1310:
	s_nop 0
	v_mov_b64_e32 v[94:95], s[18:19]
	v_cvt_pk_bf16_f32 v86, v86, v87
	v_cvt_pk_bf16_f32 v87, v88, v89
	v_cvt_pk_bf16_f32 v88, v82, v83
	v_add_u32_e32 v82, 0xa0, v147
	v_mad_i64_i32 v[90:91], s[0:1], v90, s52, v[94:95]
	v_lshlrev_b32_e32 v83, 8, v82
	v_lshl_add_u64 v[90:91], v[160:161], 1, v[90:91]
	v_cvt_pk_bf16_f32 v89, v84, v85
	s_and_b64 vcc, exec, s[6:7]
	v_and_b32_e32 v84, 0xfef00, v83
	global_store_dwordx4 v[90:91], v[86:89], off sc1
	s_cbranch_vccnz .LBB0_1312
	v_mov_b32_e32 v85, v139
	v_lshl_add_u64 v[86:87], s[20:21], 0, v[84:85]
	v_lshl_add_u64 v[86:87], s[14:15], 2, v[86:87]
	v_mov_b32_e32 v157, v139
	v_lshl_add_u64 v[110:111], v[86:87], 0, v[156:157]
	global_load_dwordx4 v[86:89], v[110:111], off offset:-512
	global_load_dwordx4 v[94:97], v[110:111], off offset:-496
	global_load_dwordx4 v[102:105], v[110:111], off offset:-480
	s_nop 0
	global_load_dwordx4 v[110:113], v[110:111], off offset:-464
	v_mov_b32_e32 v83, v78
	v_mov_b32_e32 v85, v78
	v_mov_b32_e32 v93, v79
	v_mov_b32_e32 v101, v79
	v_mov_b32_e32 v109, v80
	v_mov_b32_e32 v117, v80
	v_mov_b32_e32 v120, v81
	v_mov_b32_e32 v121, v81
	v_mov_b32_e32 v125, v74
	v_mov_b32_e32 v126, v74
	v_mov_b32_e32 v127, v75
	v_mov_b32_e32 v128, v75
	v_mov_b32_e32 v149, v76
	v_mov_b32_e32 v151, v76
	v_mov_b32_e32 v129, v77
	v_mov_b32_e32 v153, v77
	v_permlane32_swap_b32_e32 v83, v85
	v_permlane32_swap_b32_e32 v93, v101
	v_permlane32_swap_b32_e32 v109, v117
	v_permlane32_swap_b32_e32 v120, v121
	v_permlane32_swap_b32_e32 v125, v126
	v_permlane32_swap_b32_e32 v127, v128
	v_permlane32_swap_b32_e32 v149, v151
	v_permlane32_swap_b32_e32 v129, v153
	v_cndmask_b32_e64 v119, v101, v93, s[2:3]
	v_cndmask_b32_e64 v118, v85, v83, s[2:3]
	v_cndmask_b32_e64 v121, v121, v120, s[2:3]
	v_cndmask_b32_e64 v120, v117, v109, s[2:3]
	v_cndmask_b32_e64 v127, v128, v127, s[2:3]
	v_cndmask_b32_e64 v126, v126, v125, s[2:3]
	v_cndmask_b32_e64 v129, v153, v129, s[2:3]
	v_cndmask_b32_e64 v128, v151, v149, s[2:3]
	s_waitcnt vmcnt(0)
	v_mov_b32_e32 v163, v88
	v_mov_b32_e32 v88, v87
	v_mov_b32_e32 v87, v96
	v_mov_b32_e32 v96, v95
	v_mov_b32_e32 v95, v104
	v_mov_b32_e32 v104, v103
	v_mov_b32_e32 v103, v112
	v_mov_b32_e32 v112, v111
	v_mov_b32_e32 v162, v86
	v_mov_b32_e32 v86, v94
	v_mov_b32_e32 v94, v102
	v_mov_b32_e32 v102, v110
	v_pk_mul_f32 v[88:89], v[88:89], v[118:119]
	v_pk_mul_f32 v[96:97], v[96:97], v[120:121]
	v_pk_mul_f32 v[104:105], v[104:105], v[126:127]
	v_pk_mul_f32 v[110:111], v[112:113], v[128:129]
	v_cndmask_b32_e64 v89, -v89, v89, s[2:3]
	v_cndmask_b32_e64 v88, -v88, v88, s[2:3]
	v_cndmask_b32_e64 v97, -v97, v97, s[2:3]
	v_cndmask_b32_e64 v96, -v96, v96, s[2:3]
	v_cndmask_b32_e64 v105, -v105, v105, s[2:3]
	v_cndmask_b32_e64 v104, -v104, v104, s[2:3]
	v_cndmask_b32_e64 v111, -v111, v111, s[2:3]
	v_cndmask_b32_e64 v110, -v110, v110, s[2:3]
	v_pk_fma_f32 v[78:79], v[78:79], v[162:163], v[88:89]
	v_pk_fma_f32 v[80:81], v[80:81], v[86:87], v[96:97]
	v_pk_fma_f32 v[74:75], v[74:75], v[94:95], v[104:105]
	v_pk_fma_f32 v[76:77], v[76:77], v[102:103], v[110:111]
.LBB0_1312:
	s_nop 0
	v_mov_b64_e32 v[86:87], s[18:19]
	v_cvt_pk_bf16_f32 v78, v78, v79
	v_cvt_pk_bf16_f32 v79, v80, v81
	v_cvt_pk_bf16_f32 v80, v74, v75
	v_add_u32_e32 v74, 0xb0, v147
	v_mad_i64_i32 v[82:83], s[0:1], v82, s52, v[86:87]
	v_lshlrev_b32_e32 v75, 8, v74
	v_lshl_add_u64 v[82:83], v[160:161], 1, v[82:83]
	v_cvt_pk_bf16_f32 v81, v76, v77
	s_and_b64 vcc, exec, s[6:7]
	v_and_b32_e32 v76, 0xfff00, v75
	global_store_dwordx4 v[82:83], v[78:81], off sc1
	s_cbranch_vccnz .LBB0_1314
	v_mov_b32_e32 v77, v139
	v_lshl_add_u64 v[78:79], s[20:21], 0, v[76:77]
	v_lshl_add_u64 v[78:79], s[14:15], 2, v[78:79]
	v_mov_b32_e32 v157, v139
	v_lshl_add_u64 v[102:103], v[78:79], 0, v[156:157]
	global_load_dwordx4 v[78:81], v[102:103], off offset:-512
	global_load_dwordx4 v[86:89], v[102:103], off offset:-496
	global_load_dwordx4 v[94:97], v[102:103], off offset:-480
	s_nop 0
	global_load_dwordx4 v[102:105], v[102:103], off offset:-464
	v_mov_b32_e32 v75, v70
	v_mov_b32_e32 v77, v70
	v_mov_b32_e32 v85, v71
	v_mov_b32_e32 v93, v71
	v_mov_b32_e32 v101, v72
	v_mov_b32_e32 v109, v72
	v_mov_b32_e32 v112, v73
	v_mov_b32_e32 v113, v73
	v_mov_b32_e32 v117, v66
	v_mov_b32_e32 v118, v66
	v_mov_b32_e32 v119, v67
	v_mov_b32_e32 v120, v67
	v_mov_b32_e32 v125, v68
	v_mov_b32_e32 v126, v68
	v_mov_b32_e32 v121, v69
	v_mov_b32_e32 v127, v69
	v_permlane32_swap_b32_e32 v75, v77
	v_permlane32_swap_b32_e32 v85, v93
	v_permlane32_swap_b32_e32 v101, v109
	v_permlane32_swap_b32_e32 v112, v113
	v_permlane32_swap_b32_e32 v117, v118
	v_permlane32_swap_b32_e32 v119, v120
	v_permlane32_swap_b32_e32 v125, v126
	v_permlane32_swap_b32_e32 v121, v127
	v_cndmask_b32_e64 v111, v93, v85, s[2:3]
	v_cndmask_b32_e64 v110, v77, v75, s[2:3]
	v_cndmask_b32_e64 v113, v113, v112, s[2:3]
	v_cndmask_b32_e64 v112, v109, v101, s[2:3]
	v_cndmask_b32_e64 v119, v120, v119, s[2:3]
	v_cndmask_b32_e64 v118, v118, v117, s[2:3]
	v_cndmask_b32_e64 v121, v127, v121, s[2:3]
	v_cndmask_b32_e64 v120, v126, v125, s[2:3]
	s_waitcnt vmcnt(0)
	v_mov_b32_e32 v127, v80
	v_mov_b32_e32 v80, v79
	v_mov_b32_e32 v79, v88
	v_mov_b32_e32 v88, v87
	v_mov_b32_e32 v87, v96
	v_mov_b32_e32 v96, v95
	v_mov_b32_e32 v95, v104
	v_mov_b32_e32 v104, v103
	v_mov_b32_e32 v126, v78
	v_mov_b32_e32 v78, v86
	v_mov_b32_e32 v86, v94
	v_mov_b32_e32 v94, v102
	v_pk_mul_f32 v[80:81], v[80:81], v[110:111]
	v_pk_mul_f32 v[88:89], v[88:89], v[112:113]
	v_pk_mul_f32 v[96:97], v[96:97], v[118:119]
	v_pk_mul_f32 v[102:103], v[104:105], v[120:121]
	v_cndmask_b32_e64 v81, -v81, v81, s[2:3]
	v_cndmask_b32_e64 v80, -v80, v80, s[2:3]
	v_cndmask_b32_e64 v89, -v89, v89, s[2:3]
	v_cndmask_b32_e64 v88, -v88, v88, s[2:3]
	v_cndmask_b32_e64 v97, -v97, v97, s[2:3]
	v_cndmask_b32_e64 v96, -v96, v96, s[2:3]
	v_cndmask_b32_e64 v103, -v103, v103, s[2:3]
	v_cndmask_b32_e64 v102, -v102, v102, s[2:3]
	v_pk_fma_f32 v[70:71], v[70:71], v[126:127], v[80:81]
	v_pk_fma_f32 v[72:73], v[72:73], v[78:79], v[88:89]
	v_pk_fma_f32 v[66:67], v[66:67], v[86:87], v[96:97]
	v_pk_fma_f32 v[68:69], v[68:69], v[94:95], v[102:103]
.LBB0_1314:
	s_nop 0
	v_mov_b64_e32 v[78:79], s[18:19]
	v_mad_i64_i32 v[74:75], s[0:1], v74, s52, v[78:79]
	s_or_b32 s0, s30, 4
	s_mul_hi_i32 s1, s0, 0x2aaaaaab
	s_lshr_b32 s6, s1, 31
	s_add_i32 s1, s1, s6
	s_mul_i32 s1, s1, 6
	s_sub_i32 s6, s0, s1
	s_cmp_gt_i32 s6, 3
	s_cselect_b64 s[0:1], -1, 0
	s_lshl_b32 s14, s6, 5
	v_lshl_add_u64 v[74:75], v[160:161], 1, v[74:75]
	s_cmp_lt_i32 s6, 4
	v_cvt_pk_bf16_f32 v70, v70, v71
	v_cvt_pk_bf16_f32 v71, v72, v73
	v_cvt_pk_bf16_f32 v72, v66, v67
	v_cvt_pk_bf16_f32 v73, v68, v69
	global_store_dwordx4 v[74:75], v[70:73], off sc1
	s_cbranch_scc1 .LBB0_1316
	v_lshl_add_u64 v[66:67], s[20:21], 0, v[138:139]
	v_lshl_add_u64 v[66:67], s[14:15], 2, v[66:67]
	v_mov_b32_e32 v157, v139
	v_lshl_add_u64 v[86:87], v[66:67], 0, v[156:157]
	global_load_dwordx4 v[66:69], v[86:87], off offset:-512
	global_load_dwordx4 v[70:73], v[86:87], off offset:-496
	global_load_dwordx4 v[78:81], v[86:87], off offset:-480
	s_nop 0
	global_load_dwordx4 v[86:89], v[86:87], off offset:-464
	v_mov_b32_e32 v77, v62
	v_mov_b32_e32 v85, v62
	v_mov_b32_e32 v93, v63
	v_mov_b32_e32 v94, v63
	v_mov_b32_e32 v96, v64
	v_mov_b32_e32 v101, v64
	v_mov_b32_e32 v97, v65
	v_mov_b32_e32 v102, v65
	v_mov_b32_e32 v104, v58
	v_mov_b32_e32 v105, v58
	v_mov_b32_e32 v103, v59
	v_mov_b32_e32 v109, v59
	v_mov_b32_e32 v110, v60
	v_mov_b32_e32 v111, v60
	v_mov_b32_e32 v112, v61
	v_mov_b32_e32 v113, v61
	v_permlane32_swap_b32_e32 v77, v85
	v_permlane32_swap_b32_e32 v93, v94
	v_permlane32_swap_b32_e32 v96, v101
	v_permlane32_swap_b32_e32 v97, v102
	v_permlane32_swap_b32_e32 v104, v105
	v_permlane32_swap_b32_e32 v103, v109
	v_permlane32_swap_b32_e32 v110, v111
	v_permlane32_swap_b32_e32 v112, v113
	v_cndmask_b32_e64 v95, v94, v93, s[2:3]
	v_cndmask_b32_e64 v94, v85, v77, s[2:3]
	v_cndmask_b32_e64 v97, v102, v97, s[2:3]
	v_cndmask_b32_e64 v96, v101, v96, s[2:3]
	v_cndmask_b32_e64 v103, v109, v103, s[2:3]
	v_cndmask_b32_e64 v102, v105, v104, s[2:3]
	v_cndmask_b32_e64 v105, v113, v112, s[2:3]
	v_cndmask_b32_e64 v104, v111, v110, s[2:3]
	s_waitcnt vmcnt(0)
	v_mov_b32_e32 v111, v68
	v_mov_b32_e32 v68, v67
	v_mov_b32_e32 v67, v72
	v_mov_b32_e32 v72, v71
	v_mov_b32_e32 v71, v80
	v_mov_b32_e32 v80, v79
	v_mov_b32_e32 v79, v88
	v_mov_b32_e32 v88, v87
	v_mov_b32_e32 v110, v66
	v_mov_b32_e32 v66, v70
	v_mov_b32_e32 v70, v78
	v_mov_b32_e32 v78, v86
	v_pk_mul_f32 v[68:69], v[68:69], v[94:95]
	v_pk_mul_f32 v[72:73], v[72:73], v[96:97]
	v_pk_mul_f32 v[80:81], v[80:81], v[102:103]
	v_pk_mul_f32 v[86:87], v[88:89], v[104:105]
	v_cndmask_b32_e64 v69, -v69, v69, s[2:3]
	v_cndmask_b32_e64 v68, -v68, v68, s[2:3]
	v_cndmask_b32_e64 v73, -v73, v73, s[2:3]
	v_cndmask_b32_e64 v72, -v72, v72, s[2:3]
	v_cndmask_b32_e64 v81, -v81, v81, s[2:3]
	v_cndmask_b32_e64 v80, -v80, v80, s[2:3]
	v_cndmask_b32_e64 v87, -v87, v87, s[2:3]
	v_cndmask_b32_e64 v86, -v86, v86, s[2:3]
	v_pk_fma_f32 v[62:63], v[62:63], v[110:111], v[68:69]
	v_pk_fma_f32 v[64:65], v[64:65], v[66:67], v[72:73]
	v_pk_fma_f32 v[58:59], v[58:59], v[70:71], v[80:81]
	v_pk_fma_f32 v[60:61], v[60:61], v[78:79], v[86:87]
.LBB0_1316:
	v_cvt_pk_bf16_f32 v62, v62, v63
	v_cvt_pk_bf16_f32 v63, v64, v65
	v_cvt_pk_bf16_f32 v64, v58, v59
	v_cndmask_b32_e64 v58, 0, 1, s[0:1]
	v_cmp_ne_u32_e64 s[6:7], 1, v58
	s_andn2_b64 vcc, exec, s[0:1]
	v_cvt_pk_bf16_f32 v65, v60, v61
	global_store_dwordx4 v[158:159], v[62:65], off offset:256 sc1
	s_cbranch_vccnz .LBB0_1318
	v_mov_b32_e32 v125, v139
	v_lshl_add_u64 v[58:59], s[20:21], 0, v[124:125]
	v_lshl_add_u64 v[58:59], s[14:15], 2, v[58:59]
	v_mov_b32_e32 v157, v139
	v_lshl_add_u64 v[70:71], v[58:59], 0, v[156:157]
	global_load_dwordx4 v[58:61], v[70:71], off offset:-512
	global_load_dwordx4 v[62:65], v[70:71], off offset:-496
	global_load_dwordx4 v[66:69], v[70:71], off offset:-480
	s_nop 0
	global_load_dwordx4 v[70:73], v[70:71], off offset:-464
	v_mov_b32_e32 v77, v54
	v_mov_b32_e32 v78, v54
	v_mov_b32_e32 v79, v55
	v_mov_b32_e32 v80, v55
	v_mov_b32_e32 v85, v56
	v_mov_b32_e32 v86, v56
	v_mov_b32_e32 v81, v57
	v_mov_b32_e32 v87, v57
	v_mov_b32_e32 v88, v50
	v_mov_b32_e32 v89, v50
	v_mov_b32_e32 v93, v51
	v_mov_b32_e32 v94, v51
	v_mov_b32_e32 v95, v52
	v_mov_b32_e32 v96, v52
	v_mov_b32_e32 v97, v53
	v_mov_b32_e32 v101, v53
	v_permlane32_swap_b32_e32 v77, v78
	v_permlane32_swap_b32_e32 v79, v80
	v_permlane32_swap_b32_e32 v85, v86
	v_permlane32_swap_b32_e32 v81, v87
	v_permlane32_swap_b32_e32 v88, v89
	v_permlane32_swap_b32_e32 v93, v94
	v_permlane32_swap_b32_e32 v95, v96
	v_permlane32_swap_b32_e32 v97, v101
	v_cndmask_b32_e64 v79, v80, v79, s[2:3]
	v_cndmask_b32_e64 v78, v78, v77, s[2:3]
	v_cndmask_b32_e64 v81, v87, v81, s[2:3]
	v_cndmask_b32_e64 v80, v86, v85, s[2:3]
	v_cndmask_b32_e64 v87, v94, v93, s[2:3]
	v_cndmask_b32_e64 v86, v89, v88, s[2:3]
	v_cndmask_b32_e64 v89, v101, v97, s[2:3]
	v_cndmask_b32_e64 v88, v96, v95, s[2:3]
	s_waitcnt vmcnt(0)
	v_mov_b32_e32 v95, v60
	v_mov_b32_e32 v60, v59
	v_mov_b32_e32 v59, v64
	v_mov_b32_e32 v64, v63
	v_mov_b32_e32 v63, v68
	v_mov_b32_e32 v68, v67
	v_mov_b32_e32 v67, v72
	v_mov_b32_e32 v72, v71
	v_mov_b32_e32 v94, v58
	v_mov_b32_e32 v58, v62
	v_mov_b32_e32 v62, v66
	v_mov_b32_e32 v66, v70
	v_pk_mul_f32 v[60:61], v[60:61], v[78:79]
	v_pk_mul_f32 v[64:65], v[64:65], v[80:81]
	v_pk_mul_f32 v[68:69], v[68:69], v[86:87]
	v_pk_mul_f32 v[70:71], v[72:73], v[88:89]
	v_cndmask_b32_e64 v61, -v61, v61, s[2:3]
	v_cndmask_b32_e64 v60, -v60, v60, s[2:3]
	v_cndmask_b32_e64 v65, -v65, v65, s[2:3]
	v_cndmask_b32_e64 v64, -v64, v64, s[2:3]
	v_cndmask_b32_e64 v69, -v69, v69, s[2:3]
	v_cndmask_b32_e64 v68, -v68, v68, s[2:3]
	v_cndmask_b32_e64 v71, -v71, v71, s[2:3]
	v_cndmask_b32_e64 v70, -v70, v70, s[2:3]
	v_pk_fma_f32 v[54:55], v[54:55], v[94:95], v[60:61]
	v_pk_fma_f32 v[56:57], v[56:57], v[58:59], v[64:65]
	v_pk_fma_f32 v[50:51], v[50:51], v[62:63], v[68:69]
	v_pk_fma_f32 v[52:53], v[52:53], v[66:67], v[70:71]
.LBB0_1318:
	s_and_b64 vcc, exec, s[6:7]
	v_cvt_pk_bf16_f32 v54, v54, v55
	v_cvt_pk_bf16_f32 v55, v56, v57
	v_cvt_pk_bf16_f32 v56, v50, v51
	v_cvt_pk_bf16_f32 v57, v52, v53
	global_store_dwordx4 v[122:123], v[54:57], off offset:256 sc1
	s_cbranch_vccnz .LBB0_1320
	v_mov_b32_e32 v117, v139
	v_lshl_add_u64 v[50:51], s[20:21], 0, v[116:117]
	v_lshl_add_u64 v[50:51], s[14:15], 2, v[50:51]
	v_mov_b32_e32 v157, v139
	v_lshl_add_u64 v[62:63], v[50:51], 0, v[156:157]
	global_load_dwordx4 v[50:53], v[62:63], off offset:-512
	global_load_dwordx4 v[54:57], v[62:63], off offset:-496
	global_load_dwordx4 v[58:61], v[62:63], off offset:-480
	s_nop 0
	global_load_dwordx4 v[62:65], v[62:63], off offset:-464
	v_mov_b32_e32 v66, v46
	v_mov_b32_e32 v68, v46
	v_mov_b32_e32 v67, v47
	v_mov_b32_e32 v69, v47
	v_mov_b32_e32 v70, v48
	v_mov_b32_e32 v71, v48
	v_mov_b32_e32 v72, v49
	v_mov_b32_e32 v73, v49
	v_mov_b32_e32 v77, v42
	v_mov_b32_e32 v78, v42
	v_mov_b32_e32 v79, v43
	v_mov_b32_e32 v80, v43
	v_mov_b32_e32 v81, v44
	v_mov_b32_e32 v85, v44
	v_mov_b32_e32 v86, v45
	v_mov_b32_e32 v87, v45
	v_permlane32_swap_b32_e32 v66, v68
	v_permlane32_swap_b32_e32 v67, v69
	v_permlane32_swap_b32_e32 v70, v71
	v_permlane32_swap_b32_e32 v72, v73
	v_permlane32_swap_b32_e32 v77, v78
	v_permlane32_swap_b32_e32 v79, v80
	v_permlane32_swap_b32_e32 v81, v85
	v_permlane32_swap_b32_e32 v86, v87
	v_cndmask_b32_e64 v67, v69, v67, s[2:3]
	v_cndmask_b32_e64 v66, v68, v66, s[2:3]
	v_cndmask_b32_e64 v69, v73, v72, s[2:3]
	v_cndmask_b32_e64 v68, v71, v70, s[2:3]
	v_cndmask_b32_e64 v71, v80, v79, s[2:3]
	v_cndmask_b32_e64 v70, v78, v77, s[2:3]
	v_cndmask_b32_e64 v73, v87, v86, s[2:3]
	v_cndmask_b32_e64 v72, v85, v81, s[2:3]
	s_waitcnt vmcnt(0)
	v_mov_b32_e32 v79, v52
	v_mov_b32_e32 v52, v51
	v_mov_b32_e32 v51, v56
	v_mov_b32_e32 v56, v55
	v_mov_b32_e32 v55, v60
	v_mov_b32_e32 v60, v59
	v_mov_b32_e32 v59, v64
	v_mov_b32_e32 v64, v63
	v_mov_b32_e32 v78, v50
	v_mov_b32_e32 v50, v54
	v_mov_b32_e32 v54, v58
	v_mov_b32_e32 v58, v62
	v_pk_mul_f32 v[52:53], v[52:53], v[66:67]
	v_pk_mul_f32 v[56:57], v[56:57], v[68:69]
	v_pk_mul_f32 v[60:61], v[60:61], v[70:71]
	v_pk_mul_f32 v[62:63], v[64:65], v[72:73]
	v_cndmask_b32_e64 v53, -v53, v53, s[2:3]
	v_cndmask_b32_e64 v52, -v52, v52, s[2:3]
	v_cndmask_b32_e64 v57, -v57, v57, s[2:3]
	v_cndmask_b32_e64 v56, -v56, v56, s[2:3]
	v_cndmask_b32_e64 v61, -v61, v61, s[2:3]
	v_cndmask_b32_e64 v60, -v60, v60, s[2:3]
	v_cndmask_b32_e64 v63, -v63, v63, s[2:3]
	v_cndmask_b32_e64 v62, -v62, v62, s[2:3]
	v_pk_fma_f32 v[46:47], v[46:47], v[78:79], v[52:53]
	v_pk_fma_f32 v[48:49], v[48:49], v[50:51], v[56:57]
	v_pk_fma_f32 v[42:43], v[42:43], v[54:55], v[60:61]
	v_pk_fma_f32 v[44:45], v[44:45], v[58:59], v[62:63]
.LBB0_1320:
	s_and_b64 vcc, exec, s[6:7]
	v_cvt_pk_bf16_f32 v46, v46, v47
	v_cvt_pk_bf16_f32 v47, v48, v49
	v_cvt_pk_bf16_f32 v48, v42, v43
	v_cvt_pk_bf16_f32 v49, v44, v45
	global_store_dwordx4 v[114:115], v[46:49], off offset:256 sc1
	s_cbranch_vccnz .LBB0_1322
	v_mov_b32_e32 v109, v139
	v_lshl_add_u64 v[42:43], s[20:21], 0, v[108:109]
	v_lshl_add_u64 v[42:43], s[14:15], 2, v[42:43]
	v_mov_b32_e32 v157, v139
	v_lshl_add_u64 v[54:55], v[42:43], 0, v[156:157]
	global_load_dwordx4 v[42:45], v[54:55], off offset:-512
	global_load_dwordx4 v[46:49], v[54:55], off offset:-496
	global_load_dwordx4 v[50:53], v[54:55], off offset:-480
	s_nop 0
	global_load_dwordx4 v[54:57], v[54:55], off offset:-464
	v_mov_b32_e32 v58, v38
	v_mov_b32_e32 v60, v38
	v_mov_b32_e32 v59, v39
	v_mov_b32_e32 v61, v39
	v_mov_b32_e32 v62, v40
	v_mov_b32_e32 v63, v40
	v_mov_b32_e32 v64, v41
	v_mov_b32_e32 v65, v41
	v_mov_b32_e32 v66, v34
	v_mov_b32_e32 v67, v34
	v_mov_b32_e32 v68, v35
	v_mov_b32_e32 v69, v35
	v_mov_b32_e32 v70, v36
	v_mov_b32_e32 v71, v36
	v_mov_b32_e32 v72, v37
	v_mov_b32_e32 v73, v37
	v_permlane32_swap_b32_e32 v58, v60
	v_permlane32_swap_b32_e32 v59, v61
	v_permlane32_swap_b32_e32 v62, v63
	v_permlane32_swap_b32_e32 v64, v65
	v_permlane32_swap_b32_e32 v66, v67
	v_permlane32_swap_b32_e32 v68, v69
	v_permlane32_swap_b32_e32 v70, v71
	v_permlane32_swap_b32_e32 v72, v73
	v_cndmask_b32_e64 v59, v61, v59, s[2:3]
	v_cndmask_b32_e64 v58, v60, v58, s[2:3]
	v_cndmask_b32_e64 v61, v65, v64, s[2:3]
	v_cndmask_b32_e64 v60, v63, v62, s[2:3]
	v_cndmask_b32_e64 v63, v69, v68, s[2:3]
	v_cndmask_b32_e64 v62, v67, v66, s[2:3]
	v_cndmask_b32_e64 v65, v73, v72, s[2:3]
	v_cndmask_b32_e64 v64, v71, v70, s[2:3]
	s_waitcnt vmcnt(0)
	v_mov_b32_e32 v67, v44
	v_mov_b32_e32 v44, v43
	v_mov_b32_e32 v43, v48
	v_mov_b32_e32 v48, v47
	v_mov_b32_e32 v47, v52
	v_mov_b32_e32 v52, v51
	v_mov_b32_e32 v51, v56
	v_mov_b32_e32 v56, v55
	v_mov_b32_e32 v66, v42
	v_mov_b32_e32 v42, v46
	v_mov_b32_e32 v46, v50
	v_mov_b32_e32 v50, v54
	v_pk_mul_f32 v[44:45], v[44:45], v[58:59]
	v_pk_mul_f32 v[48:49], v[48:49], v[60:61]
	v_pk_mul_f32 v[52:53], v[52:53], v[62:63]
	v_pk_mul_f32 v[54:55], v[56:57], v[64:65]
	v_cndmask_b32_e64 v45, -v45, v45, s[2:3]
	v_cndmask_b32_e64 v44, -v44, v44, s[2:3]
	v_cndmask_b32_e64 v49, -v49, v49, s[2:3]
	v_cndmask_b32_e64 v48, -v48, v48, s[2:3]
	v_cndmask_b32_e64 v53, -v53, v53, s[2:3]
	v_cndmask_b32_e64 v52, -v52, v52, s[2:3]
	v_cndmask_b32_e64 v55, -v55, v55, s[2:3]
	v_cndmask_b32_e64 v54, -v54, v54, s[2:3]
	v_pk_fma_f32 v[38:39], v[38:39], v[66:67], v[44:45]
	v_pk_fma_f32 v[40:41], v[40:41], v[42:43], v[48:49]
	v_pk_fma_f32 v[34:35], v[34:35], v[46:47], v[52:53]
	v_pk_fma_f32 v[36:37], v[36:37], v[50:51], v[54:55]
.LBB0_1322:
	s_and_b64 vcc, exec, s[6:7]
	v_cvt_pk_bf16_f32 v38, v38, v39
	v_cvt_pk_bf16_f32 v39, v40, v41
	v_cvt_pk_bf16_f32 v40, v34, v35
	v_cvt_pk_bf16_f32 v41, v36, v37
	global_store_dwordx4 v[106:107], v[38:41], off offset:256 sc1
	s_cbranch_vccnz .LBB0_1324
	v_mov_b32_e32 v101, v139
	v_lshl_add_u64 v[34:35], s[20:21], 0, v[100:101]
	v_lshl_add_u64 v[34:35], s[14:15], 2, v[34:35]
	v_mov_b32_e32 v157, v139
	v_lshl_add_u64 v[46:47], v[34:35], 0, v[156:157]
	global_load_dwordx4 v[34:37], v[46:47], off offset:-512
	global_load_dwordx4 v[38:41], v[46:47], off offset:-496
	global_load_dwordx4 v[42:45], v[46:47], off offset:-480
	s_nop 0
	global_load_dwordx4 v[46:49], v[46:47], off offset:-464
	v_mov_b32_e32 v50, v30
	v_mov_b32_e32 v52, v30
	v_mov_b32_e32 v51, v31
	v_mov_b32_e32 v53, v31
	v_mov_b32_e32 v54, v32
	v_mov_b32_e32 v55, v32
	v_mov_b32_e32 v56, v33
	v_mov_b32_e32 v57, v33
	v_mov_b32_e32 v58, v26
	v_mov_b32_e32 v59, v26
	v_mov_b32_e32 v60, v27
	v_mov_b32_e32 v61, v27
	v_mov_b32_e32 v62, v28
	v_mov_b32_e32 v63, v28
	v_mov_b32_e32 v64, v29
	v_mov_b32_e32 v65, v29
	v_permlane32_swap_b32_e32 v50, v52
	v_permlane32_swap_b32_e32 v51, v53
	v_permlane32_swap_b32_e32 v54, v55
	v_permlane32_swap_b32_e32 v56, v57
	v_permlane32_swap_b32_e32 v58, v59
	v_permlane32_swap_b32_e32 v60, v61
	v_permlane32_swap_b32_e32 v62, v63
	v_permlane32_swap_b32_e32 v64, v65
	v_cndmask_b32_e64 v51, v53, v51, s[2:3]
	v_cndmask_b32_e64 v50, v52, v50, s[2:3]
	v_cndmask_b32_e64 v53, v57, v56, s[2:3]
	v_cndmask_b32_e64 v52, v55, v54, s[2:3]
	v_cndmask_b32_e64 v55, v61, v60, s[2:3]
	v_cndmask_b32_e64 v54, v59, v58, s[2:3]
	v_cndmask_b32_e64 v57, v65, v64, s[2:3]
	v_cndmask_b32_e64 v56, v63, v62, s[2:3]
	s_waitcnt vmcnt(0)
	v_mov_b32_e32 v59, v36
	v_mov_b32_e32 v36, v35
	v_mov_b32_e32 v35, v40
	v_mov_b32_e32 v40, v39
	v_mov_b32_e32 v39, v44
	v_mov_b32_e32 v44, v43
	v_mov_b32_e32 v43, v48
	v_mov_b32_e32 v48, v47
	v_mov_b32_e32 v58, v34
	v_mov_b32_e32 v34, v38
	v_mov_b32_e32 v38, v42
	v_mov_b32_e32 v42, v46
	v_pk_mul_f32 v[36:37], v[36:37], v[50:51]
	v_pk_mul_f32 v[40:41], v[40:41], v[52:53]
	v_pk_mul_f32 v[44:45], v[44:45], v[54:55]
	v_pk_mul_f32 v[46:47], v[48:49], v[56:57]
	v_cndmask_b32_e64 v37, -v37, v37, s[2:3]
	v_cndmask_b32_e64 v36, -v36, v36, s[2:3]
	v_cndmask_b32_e64 v41, -v41, v41, s[2:3]
	v_cndmask_b32_e64 v40, -v40, v40, s[2:3]
	v_cndmask_b32_e64 v45, -v45, v45, s[2:3]
	v_cndmask_b32_e64 v44, -v44, v44, s[2:3]
	v_cndmask_b32_e64 v47, -v47, v47, s[2:3]
	v_cndmask_b32_e64 v46, -v46, v46, s[2:3]
	v_pk_fma_f32 v[30:31], v[30:31], v[58:59], v[36:37]
	v_pk_fma_f32 v[32:33], v[32:33], v[34:35], v[40:41]
	v_pk_fma_f32 v[26:27], v[26:27], v[38:39], v[44:45]
	v_pk_fma_f32 v[28:29], v[28:29], v[42:43], v[46:47]
.LBB0_1324:
	s_and_b64 vcc, exec, s[6:7]
	v_cvt_pk_bf16_f32 v30, v30, v31
	v_cvt_pk_bf16_f32 v31, v32, v33
	v_cvt_pk_bf16_f32 v32, v26, v27
	v_cvt_pk_bf16_f32 v33, v28, v29
	global_store_dwordx4 v[98:99], v[30:33], off offset:256 sc1
	s_cbranch_vccnz .LBB0_1326
	v_mov_b32_e32 v93, v139
	v_lshl_add_u64 v[26:27], s[20:21], 0, v[92:93]
	v_lshl_add_u64 v[26:27], s[14:15], 2, v[26:27]
	v_mov_b32_e32 v157, v139
	v_lshl_add_u64 v[38:39], v[26:27], 0, v[156:157]
	global_load_dwordx4 v[26:29], v[38:39], off offset:-512
	global_load_dwordx4 v[30:33], v[38:39], off offset:-496
	global_load_dwordx4 v[34:37], v[38:39], off offset:-480
	s_nop 0
	global_load_dwordx4 v[38:41], v[38:39], off offset:-464
	v_mov_b32_e32 v42, v22
	v_mov_b32_e32 v44, v22
	v_mov_b32_e32 v43, v23
	v_mov_b32_e32 v45, v23
	v_mov_b32_e32 v46, v24
	v_mov_b32_e32 v47, v24
	v_mov_b32_e32 v48, v25
	v_mov_b32_e32 v49, v25
	v_mov_b32_e32 v50, v18
	v_mov_b32_e32 v51, v18
	v_mov_b32_e32 v52, v19
	v_mov_b32_e32 v53, v19
	v_mov_b32_e32 v54, v20
	v_mov_b32_e32 v55, v20
	v_mov_b32_e32 v56, v21
	v_mov_b32_e32 v57, v21
	v_permlane32_swap_b32_e32 v42, v44
	v_permlane32_swap_b32_e32 v43, v45
	v_permlane32_swap_b32_e32 v46, v47
	v_permlane32_swap_b32_e32 v48, v49
	v_permlane32_swap_b32_e32 v50, v51
	v_permlane32_swap_b32_e32 v52, v53
	v_permlane32_swap_b32_e32 v54, v55
	v_permlane32_swap_b32_e32 v56, v57
	v_cndmask_b32_e64 v43, v45, v43, s[2:3]
	v_cndmask_b32_e64 v42, v44, v42, s[2:3]
	v_cndmask_b32_e64 v45, v49, v48, s[2:3]
	v_cndmask_b32_e64 v44, v47, v46, s[2:3]
	v_cndmask_b32_e64 v47, v53, v52, s[2:3]
	v_cndmask_b32_e64 v46, v51, v50, s[2:3]
	v_cndmask_b32_e64 v49, v57, v56, s[2:3]
	v_cndmask_b32_e64 v48, v55, v54, s[2:3]
	s_waitcnt vmcnt(0)
	v_mov_b32_e32 v51, v28
	v_mov_b32_e32 v28, v27
	v_mov_b32_e32 v27, v32
	v_mov_b32_e32 v32, v31
	v_mov_b32_e32 v31, v36
	v_mov_b32_e32 v36, v35
	v_mov_b32_e32 v35, v40
	v_mov_b32_e32 v40, v39
	v_mov_b32_e32 v50, v26
	v_mov_b32_e32 v26, v30
	v_mov_b32_e32 v30, v34
	v_mov_b32_e32 v34, v38
	v_pk_mul_f32 v[28:29], v[28:29], v[42:43]
	v_pk_mul_f32 v[32:33], v[32:33], v[44:45]
	v_pk_mul_f32 v[36:37], v[36:37], v[46:47]
	v_pk_mul_f32 v[38:39], v[40:41], v[48:49]
	v_cndmask_b32_e64 v29, -v29, v29, s[2:3]
	v_cndmask_b32_e64 v28, -v28, v28, s[2:3]
	v_cndmask_b32_e64 v33, -v33, v33, s[2:3]
	v_cndmask_b32_e64 v32, -v32, v32, s[2:3]
	v_cndmask_b32_e64 v37, -v37, v37, s[2:3]
	v_cndmask_b32_e64 v36, -v36, v36, s[2:3]
	v_cndmask_b32_e64 v39, -v39, v39, s[2:3]
	v_cndmask_b32_e64 v38, -v38, v38, s[2:3]
	v_pk_fma_f32 v[22:23], v[22:23], v[50:51], v[28:29]
	v_pk_fma_f32 v[24:25], v[24:25], v[26:27], v[32:33]
	v_pk_fma_f32 v[18:19], v[18:19], v[30:31], v[36:37]
	v_pk_fma_f32 v[20:21], v[20:21], v[34:35], v[38:39]
.LBB0_1326:
	s_and_b64 vcc, exec, s[6:7]
	v_cvt_pk_bf16_f32 v22, v22, v23
	v_cvt_pk_bf16_f32 v23, v24, v25
	v_cvt_pk_bf16_f32 v24, v18, v19
	v_cvt_pk_bf16_f32 v25, v20, v21
	global_store_dwordx4 v[90:91], v[22:25], off offset:256 sc1
	s_cbranch_vccnz .LBB0_1328
	v_mov_b32_e32 v85, v139
	v_lshl_add_u64 v[18:19], s[20:21], 0, v[84:85]
	v_lshl_add_u64 v[18:19], s[14:15], 2, v[18:19]
	v_mov_b32_e32 v157, v139
	v_lshl_add_u64 v[30:31], v[18:19], 0, v[156:157]
	global_load_dwordx4 v[18:21], v[30:31], off offset:-512
	global_load_dwordx4 v[22:25], v[30:31], off offset:-496
	global_load_dwordx4 v[26:29], v[30:31], off offset:-480
	s_nop 0
	global_load_dwordx4 v[30:33], v[30:31], off offset:-464
	v_mov_b32_e32 v34, v10
	v_mov_b32_e32 v36, v10
	v_mov_b32_e32 v35, v11
	v_mov_b32_e32 v37, v11
	v_mov_b32_e32 v38, v12
	v_mov_b32_e32 v39, v12
	v_mov_b32_e32 v40, v13
	v_mov_b32_e32 v41, v13
	v_mov_b32_e32 v42, v14
	v_mov_b32_e32 v43, v14
	v_mov_b32_e32 v44, v15
	v_mov_b32_e32 v45, v15
	v_mov_b32_e32 v46, v16
	v_mov_b32_e32 v47, v16
	v_mov_b32_e32 v48, v17
	v_mov_b32_e32 v49, v17
	v_permlane32_swap_b32_e32 v34, v36
	v_permlane32_swap_b32_e32 v35, v37
	v_permlane32_swap_b32_e32 v38, v39
	v_permlane32_swap_b32_e32 v40, v41
	v_permlane32_swap_b32_e32 v42, v43
	v_permlane32_swap_b32_e32 v44, v45
	v_permlane32_swap_b32_e32 v46, v47
	v_permlane32_swap_b32_e32 v48, v49
	v_cndmask_b32_e64 v35, v37, v35, s[2:3]
	v_cndmask_b32_e64 v34, v36, v34, s[2:3]
	v_cndmask_b32_e64 v37, v41, v40, s[2:3]
	v_cndmask_b32_e64 v36, v39, v38, s[2:3]
	v_cndmask_b32_e64 v39, v45, v44, s[2:3]
	v_cndmask_b32_e64 v38, v43, v42, s[2:3]
	v_cndmask_b32_e64 v41, v49, v48, s[2:3]
	v_cndmask_b32_e64 v40, v47, v46, s[2:3]
	s_waitcnt vmcnt(0)
	v_mov_b32_e32 v43, v20
	v_mov_b32_e32 v20, v19
	v_mov_b32_e32 v19, v24
	v_mov_b32_e32 v24, v23
	v_mov_b32_e32 v23, v28
	v_mov_b32_e32 v28, v27
	v_mov_b32_e32 v27, v32
	v_mov_b32_e32 v32, v31
	v_mov_b32_e32 v42, v18
	v_mov_b32_e32 v18, v22
	v_mov_b32_e32 v22, v26
	v_mov_b32_e32 v26, v30
	v_pk_mul_f32 v[20:21], v[20:21], v[34:35]
	v_pk_mul_f32 v[24:25], v[24:25], v[36:37]
	v_pk_mul_f32 v[28:29], v[28:29], v[38:39]
	v_pk_mul_f32 v[30:31], v[32:33], v[40:41]
	v_cndmask_b32_e64 v21, -v21, v21, s[2:3]
	v_cndmask_b32_e64 v20, -v20, v20, s[2:3]
	v_cndmask_b32_e64 v25, -v25, v25, s[2:3]
	v_cndmask_b32_e64 v24, -v24, v24, s[2:3]
	v_cndmask_b32_e64 v29, -v29, v29, s[2:3]
	v_cndmask_b32_e64 v28, -v28, v28, s[2:3]
	v_cndmask_b32_e64 v31, -v31, v31, s[2:3]
	v_cndmask_b32_e64 v30, -v30, v30, s[2:3]
	v_pk_fma_f32 v[10:11], v[10:11], v[42:43], v[20:21]
	v_pk_fma_f32 v[12:13], v[12:13], v[18:19], v[24:25]
	v_pk_fma_f32 v[14:15], v[14:15], v[22:23], v[28:29]
	v_pk_fma_f32 v[16:17], v[16:17], v[26:27], v[30:31]
.LBB0_1328:
	s_and_b64 vcc, exec, s[6:7]
	v_cvt_pk_bf16_f32 v10, v10, v11
	v_cvt_pk_bf16_f32 v11, v12, v13
	v_cvt_pk_bf16_f32 v12, v14, v15
	v_cvt_pk_bf16_f32 v13, v16, v17
	global_store_dwordx4 v[82:83], v[10:13], off offset:256 sc1
	s_cbranch_vccnz .LBB0_1330
	v_mov_b32_e32 v77, v139
	v_lshl_add_u64 v[10:11], s[20:21], 0, v[76:77]
	v_lshl_add_u64 v[10:11], s[14:15], 2, v[10:11]
	v_mov_b32_e32 v157, v139
	v_lshl_add_u64 v[22:23], v[10:11], 0, v[156:157]
	global_load_dwordx4 v[10:13], v[22:23], off offset:-512
	global_load_dwordx4 v[14:17], v[22:23], off offset:-496
	global_load_dwordx4 v[18:21], v[22:23], off offset:-480
	s_nop 0
	global_load_dwordx4 v[22:25], v[22:23], off offset:-464
	v_mov_b32_e32 v26, v2
	v_mov_b32_e32 v28, v2
	v_mov_b32_e32 v27, v3
	v_mov_b32_e32 v29, v3
	v_mov_b32_e32 v30, v4
	v_mov_b32_e32 v31, v4
	v_mov_b32_e32 v32, v5
	v_mov_b32_e32 v33, v5
	v_mov_b32_e32 v34, v6
	v_mov_b32_e32 v35, v6
	v_mov_b32_e32 v36, v7
	v_mov_b32_e32 v37, v7
	v_mov_b32_e32 v38, v8
	v_mov_b32_e32 v39, v8
	v_mov_b32_e32 v40, v9
	v_mov_b32_e32 v41, v9
	v_permlane32_swap_b32_e32 v26, v28
	v_permlane32_swap_b32_e32 v27, v29
	v_permlane32_swap_b32_e32 v30, v31
	v_permlane32_swap_b32_e32 v32, v33
	v_permlane32_swap_b32_e32 v34, v35
	v_permlane32_swap_b32_e32 v36, v37
	v_permlane32_swap_b32_e32 v38, v39
	v_permlane32_swap_b32_e32 v40, v41
	v_cndmask_b32_e64 v27, v29, v27, s[2:3]
	v_cndmask_b32_e64 v26, v28, v26, s[2:3]
	v_cndmask_b32_e64 v29, v33, v32, s[2:3]
	v_cndmask_b32_e64 v28, v31, v30, s[2:3]
	v_cndmask_b32_e64 v31, v37, v36, s[2:3]
	v_cndmask_b32_e64 v30, v35, v34, s[2:3]
	v_cndmask_b32_e64 v33, v41, v40, s[2:3]
	v_cndmask_b32_e64 v32, v39, v38, s[2:3]
	s_waitcnt vmcnt(0)
	v_mov_b32_e32 v35, v12
	v_mov_b32_e32 v12, v11
	v_mov_b32_e32 v11, v16
	v_mov_b32_e32 v16, v15
	v_mov_b32_e32 v15, v20
	v_mov_b32_e32 v20, v19
	v_mov_b32_e32 v19, v24
	v_mov_b32_e32 v24, v23
	v_mov_b32_e32 v34, v10
	v_mov_b32_e32 v10, v14
	v_mov_b32_e32 v14, v18
	v_mov_b32_e32 v18, v22
	v_pk_mul_f32 v[12:13], v[12:13], v[26:27]
	v_pk_mul_f32 v[16:17], v[16:17], v[28:29]
	v_pk_mul_f32 v[20:21], v[20:21], v[30:31]
	v_pk_mul_f32 v[22:23], v[24:25], v[32:33]
	v_cndmask_b32_e64 v13, -v13, v13, s[2:3]
	v_cndmask_b32_e64 v12, -v12, v12, s[2:3]
	v_cndmask_b32_e64 v17, -v17, v17, s[2:3]
	v_cndmask_b32_e64 v16, -v16, v16, s[2:3]
	v_cndmask_b32_e64 v21, -v21, v21, s[2:3]
	v_cndmask_b32_e64 v20, -v20, v20, s[2:3]
	v_cndmask_b32_e64 v23, -v23, v23, s[2:3]
	v_cndmask_b32_e64 v22, -v22, v22, s[2:3]
	v_pk_fma_f32 v[2:3], v[2:3], v[34:35], v[12:13]
	v_pk_fma_f32 v[4:5], v[4:5], v[10:11], v[16:17]
	v_pk_fma_f32 v[6:7], v[6:7], v[14:15], v[20:21]
	v_pk_fma_f32 v[8:9], v[8:9], v[18:19], v[22:23]
.LBB0_1330:
	s_and_b64 vcc, exec, s[4:5]
	s_mov_b64 s[0:1], -1
	v_cvt_pk_bf16_f32 v2, v2, v3
	v_cvt_pk_bf16_f32 v3, v4, v5
	v_cvt_pk_bf16_f32 v4, v6, v7
	v_cvt_pk_bf16_f32 v5, v8, v9
	global_store_dwordx4 v[74:75], v[2:5], off offset:256 sc1
	s_cbranch_vccnz .LBB0_1289
	s_andn2_b64 vcc, exec, s[16:17]
	s_cbranch_vccnz .LBB0_1288
	s_barrier
	s_branch .LBB0_1288

.LBB0_1348:
	v_lshl_add_u32 v142, s55, 8, v153
	v_lshl_or_b32 v140, s56, 8, v156
	v_ashrrev_i32_e32 v143, 31, v142
	v_ashrrev_i32_e32 v141, 31, v140
	v_lshlrev_b64 v[144:145], 13, v[142:143]
	v_lshl_add_u64 v[144:145], s[10:11], 0, v[144:145]
	v_lshlrev_b64 v[146:147], 1, v[140:141]
	v_lshl_add_u64 v[140:141], v[144:145], 0, v[146:147]
	v_cvt_pk_bf16_f32 v126, v126, v127
	v_cvt_pk_bf16_f32 v127, v128, v129
	v_cvt_pk_bf16_f32 v128, v122, v123
	v_cvt_pk_bf16_f32 v129, v124, v125
	global_store_dwordx4 v[140:141], v[126:129], off sc1
	v_cvt_pk_bf16_f32 v114, v114, v115
	v_cvt_pk_bf16_f32 v115, v116, v117
	v_cvt_pk_bf16_f32 v116, v106, v107
	v_or_b32_e32 v106, 16, v142
	v_ashrrev_i32_e32 v107, 31, v106
	v_lshlrev_b64 v[106:107], 13, v[106:107]
	v_lshl_add_u64 v[106:107], s[10:11], 0, v[106:107]
	v_cvt_pk_bf16_f32 v117, v108, v109
	global_store_dwordx4 v[140:141], v[114:117], off offset:256 sc1
	s_nop 1
	v_lshl_add_u64 v[114:115], v[106:107], 0, v[146:147]
	v_cvt_pk_bf16_f32 v106, v118, v119
	v_cvt_pk_bf16_f32 v107, v120, v121
	v_cvt_pk_bf16_f32 v108, v110, v111
	v_cvt_pk_bf16_f32 v109, v112, v113
	global_store_dwordx4 v[114:115], v[106:109], off sc1
	v_cvt_pk_bf16_f32 v98, v98, v99
	v_cvt_pk_bf16_f32 v99, v100, v101
	v_cvt_pk_bf16_f32 v100, v90, v91
	v_or_b32_e32 v90, 32, v142
	v_ashrrev_i32_e32 v91, 31, v90
	v_lshlrev_b64 v[90:91], 13, v[90:91]
	v_lshl_add_u64 v[90:91], s[10:11], 0, v[90:91]
	v_cvt_pk_bf16_f32 v101, v92, v93
	global_store_dwordx4 v[114:115], v[98:101], off offset:256 sc1
	s_nop 1
	v_lshl_add_u64 v[98:99], v[90:91], 0, v[146:147]
	v_cvt_pk_bf16_f32 v90, v102, v103
	v_cvt_pk_bf16_f32 v91, v104, v105
	v_cvt_pk_bf16_f32 v92, v94, v95
	v_cvt_pk_bf16_f32 v93, v96, v97
	global_store_dwordx4 v[98:99], v[90:93], off sc1
	v_cvt_pk_bf16_f32 v82, v82, v83
	v_cvt_pk_bf16_f32 v83, v84, v85
	v_cvt_pk_bf16_f32 v84, v74, v75
	v_or_b32_e32 v74, 48, v142
	v_ashrrev_i32_e32 v75, 31, v74
	v_lshlrev_b64 v[74:75], 13, v[74:75]
	v_lshl_add_u64 v[74:75], s[10:11], 0, v[74:75]
	v_cvt_pk_bf16_f32 v85, v76, v77
	global_store_dwordx4 v[98:99], v[82:85], off offset:256 sc1
	s_nop 1
	v_lshl_add_u64 v[82:83], v[74:75], 0, v[146:147]
	v_cvt_pk_bf16_f32 v74, v86, v87
	v_cvt_pk_bf16_f32 v75, v88, v89
	v_cvt_pk_bf16_f32 v76, v78, v79
	v_cvt_pk_bf16_f32 v77, v80, v81
	global_store_dwordx4 v[82:83], v[74:77], off sc1
	v_cvt_pk_bf16_f32 v70, v70, v71
	v_cvt_pk_bf16_f32 v71, v72, v73
	v_cvt_pk_bf16_f32 v72, v66, v67
	v_cvt_pk_bf16_f32 v73, v68, v69
	global_store_dwordx4 v[82:83], v[70:73], off offset:256 sc1
	v_cvt_pk_bf16_f32 v62, v62, v63
	v_cvt_pk_bf16_f32 v63, v64, v65
	v_cvt_pk_bf16_f32 v64, v58, v59
	v_add_co_u32_e32 v58, vcc, s50, v140
	v_lshl_add_u64 v[66:67], v[140:141], 0, s[18:19]
	s_nop 0
	v_addc_co_u32_e32 v59, vcc, 0, v141, vcc
	v_cvt_pk_bf16_f32 v65, v60, v61
	global_store_dwordx4 v[58:59], v[62:65], off sc1
	v_cvt_pk_bf16_f32 v42, v42, v43
	v_cvt_pk_bf16_f32 v43, v44, v45
	v_cvt_pk_bf16_f32 v44, v30, v31
	v_cvt_pk_bf16_f32 v45, v32, v33
	global_store_dwordx4 v[66:67], v[42:45], off offset:256 sc1
	v_cvt_pk_bf16_f32 v30, v46, v47
	v_cvt_pk_bf16_f32 v31, v48, v49
	v_cvt_pk_bf16_f32 v32, v38, v39
	v_add_co_u32_e32 v38, vcc, s51, v140
	s_nop 0
	v_lshl_add_u64 v[42:43], v[140:141], 0, s[20:21]
	v_addc_co_u32_e32 v39, vcc, 0, v141, vcc
	v_cvt_pk_bf16_f32 v33, v40, v41
	global_store_dwordx4 v[38:39], v[30:33], off sc1
	v_cvt_pk_bf16_f32 v18, v18, v19
	v_cvt_pk_bf16_f32 v19, v20, v21
	v_cvt_pk_bf16_f32 v20, v10, v11
	v_cvt_pk_bf16_f32 v21, v12, v13
	global_store_dwordx4 v[42:43], v[18:21], off offset:256 sc1
	v_cvt_pk_bf16_f32 v10, v22, v23
	v_cvt_pk_bf16_f32 v11, v24, v25
	v_cvt_pk_bf16_f32 v12, v14, v15
	v_add_co_u32_e32 v14, vcc, s52, v140
	s_nop 0
	v_lshl_add_u64 v[18:19], v[140:141], 0, s[22:23]
	v_cvt_pk_bf16_f32 v13, v16, v17
	v_addc_co_u32_e32 v15, vcc, 0, v141, vcc
	global_store_dwordx4 v[14:15], v[10:13], off sc1
	s_nop 1
	v_cvt_pk_bf16_f32 v10, v54, v55
	v_cvt_pk_bf16_f32 v11, v56, v57
	v_cvt_pk_bf16_f32 v12, v50, v51
	v_cvt_pk_bf16_f32 v13, v52, v53
	global_store_dwordx4 v[18:19], v[10:13], off offset:256 sc1
	v_cvt_pk_bf16_f32 v6, v6, v7
	v_cvt_pk_bf16_f32 v7, v8, v9
	v_cvt_pk_bf16_f32 v8, v2, v3
	v_add_co_u32_e32 v2, vcc, s53, v140
	s_nop 0
	v_lshl_add_u64 v[10:11], v[140:141], 0, s[24:25]
	v_addc_co_u32_e32 v3, vcc, 0, v141, vcc
	s_and_b64 vcc, exec, s[2:3]
	s_mov_b64 s[2:3], -1
	v_cvt_pk_bf16_f32 v9, v4, v5
	global_store_dwordx4 v[2:3], v[6:9], off sc1
	v_cvt_pk_bf16_f32 v2, v34, v35
	v_cvt_pk_bf16_f32 v3, v36, v37
	v_cvt_pk_bf16_f32 v4, v26, v27
	v_cvt_pk_bf16_f32 v5, v28, v29
	global_store_dwordx4 v[10:11], v[2:5], off offset:256 sc1
	s_cbranch_vccnz .LBB0_1339
	s_andn2_b64 vcc, exec, s[0:1]
	s_cbranch_vccnz .LBB0_1338
	s_barrier
	s_branch .LBB0_1338

.LBB0_1500:
	v_lshl_add_u32 v142, s54, 8, v153
	v_lshl_or_b32 v140, s55, 8, v156
	v_ashrrev_i32_e32 v143, 31, v142
	v_ashrrev_i32_e32 v141, 31, v140
	v_lshlrev_b64 v[144:145], 12, v[142:143]
	v_lshl_add_u64 v[144:145], s[10:11], 0, v[144:145]
	v_lshlrev_b64 v[146:147], 1, v[140:141]
	v_lshl_add_u64 v[140:141], v[144:145], 0, v[146:147]
	v_cvt_pk_bf16_f32 v126, v126, v127
	v_cvt_pk_bf16_f32 v127, v128, v129
	v_cvt_pk_bf16_f32 v128, v122, v123
	v_cvt_pk_bf16_f32 v129, v124, v125
	global_store_dwordx4 v[140:141], v[126:129], off sc1
	v_cvt_pk_bf16_f32 v114, v114, v115
	v_cvt_pk_bf16_f32 v115, v116, v117
	v_cvt_pk_bf16_f32 v116, v106, v107
	v_or_b32_e32 v106, 16, v142
	v_ashrrev_i32_e32 v107, 31, v106
	v_lshlrev_b64 v[106:107], 12, v[106:107]
	v_lshl_add_u64 v[106:107], s[10:11], 0, v[106:107]
	v_cvt_pk_bf16_f32 v117, v108, v109
	global_store_dwordx4 v[140:141], v[114:117], off offset:256 sc1
	s_nop 1
	v_lshl_add_u64 v[114:115], v[106:107], 0, v[146:147]
	v_cvt_pk_bf16_f32 v106, v118, v119
	v_cvt_pk_bf16_f32 v107, v120, v121
	v_cvt_pk_bf16_f32 v108, v110, v111
	v_cvt_pk_bf16_f32 v109, v112, v113
	global_store_dwordx4 v[114:115], v[106:109], off sc1
	v_cvt_pk_bf16_f32 v98, v98, v99
	v_cvt_pk_bf16_f32 v99, v100, v101
	v_cvt_pk_bf16_f32 v100, v90, v91
	v_or_b32_e32 v90, 32, v142
	v_ashrrev_i32_e32 v91, 31, v90
	v_lshlrev_b64 v[90:91], 12, v[90:91]
	v_lshl_add_u64 v[90:91], s[10:11], 0, v[90:91]
	v_cvt_pk_bf16_f32 v101, v92, v93
	global_store_dwordx4 v[114:115], v[98:101], off offset:256 sc1
	s_nop 1
	v_lshl_add_u64 v[98:99], v[90:91], 0, v[146:147]
	v_cvt_pk_bf16_f32 v90, v102, v103
	v_cvt_pk_bf16_f32 v91, v104, v105
	v_cvt_pk_bf16_f32 v92, v94, v95
	v_cvt_pk_bf16_f32 v93, v96, v97
	global_store_dwordx4 v[98:99], v[90:93], off sc1
	v_cvt_pk_bf16_f32 v82, v82, v83
	v_cvt_pk_bf16_f32 v83, v84, v85
	v_cvt_pk_bf16_f32 v84, v74, v75
	v_or_b32_e32 v74, 48, v142
	v_ashrrev_i32_e32 v75, 31, v74
	v_lshlrev_b64 v[74:75], 12, v[74:75]
	v_lshl_add_u64 v[74:75], s[10:11], 0, v[74:75]
	v_cvt_pk_bf16_f32 v85, v76, v77
	global_store_dwordx4 v[98:99], v[82:85], off offset:256 sc1
	s_nop 1
	v_lshl_add_u64 v[82:83], v[74:75], 0, v[146:147]
	v_cvt_pk_bf16_f32 v74, v86, v87
	v_cvt_pk_bf16_f32 v75, v88, v89
	v_cvt_pk_bf16_f32 v76, v78, v79
	v_cvt_pk_bf16_f32 v77, v80, v81
	global_store_dwordx4 v[82:83], v[74:77], off sc1
	v_cvt_pk_bf16_f32 v70, v70, v71
	v_cvt_pk_bf16_f32 v71, v72, v73
	v_cvt_pk_bf16_f32 v72, v66, v67
	v_cvt_pk_bf16_f32 v73, v68, v69
	global_store_dwordx4 v[82:83], v[70:73], off offset:256 sc1
	v_cvt_pk_bf16_f32 v62, v62, v63
	v_cvt_pk_bf16_f32 v63, v64, v65
	v_cvt_pk_bf16_f32 v64, v58, v59
	v_add_co_u32_e32 v58, vcc, s49, v140
	v_lshl_add_u64 v[66:67], v[140:141], 0, s[18:19]
	s_nop 0
	v_addc_co_u32_e32 v59, vcc, 0, v141, vcc
	v_cvt_pk_bf16_f32 v65, v60, v61
	global_store_dwordx4 v[58:59], v[62:65], off sc1
	v_cvt_pk_bf16_f32 v42, v42, v43
	v_cvt_pk_bf16_f32 v43, v44, v45
	v_cvt_pk_bf16_f32 v44, v30, v31
	v_cvt_pk_bf16_f32 v45, v32, v33
	global_store_dwordx4 v[66:67], v[42:45], off offset:256 sc1
	v_cvt_pk_bf16_f32 v30, v46, v47
	v_cvt_pk_bf16_f32 v31, v48, v49
	v_cvt_pk_bf16_f32 v32, v38, v39
	v_add_co_u32_e32 v38, vcc, s50, v140
	s_nop 0
	v_lshl_add_u64 v[42:43], v[140:141], 0, s[20:21]
	v_addc_co_u32_e32 v39, vcc, 0, v141, vcc
	v_cvt_pk_bf16_f32 v33, v40, v41
	global_store_dwordx4 v[38:39], v[30:33], off sc1
	v_cvt_pk_bf16_f32 v18, v18, v19
	v_cvt_pk_bf16_f32 v19, v20, v21
	v_cvt_pk_bf16_f32 v20, v10, v11
	v_cvt_pk_bf16_f32 v21, v12, v13
	global_store_dwordx4 v[42:43], v[18:21], off offset:256 sc1
	v_cvt_pk_bf16_f32 v10, v22, v23
	v_cvt_pk_bf16_f32 v11, v24, v25
	v_cvt_pk_bf16_f32 v12, v14, v15
	v_add_co_u32_e32 v14, vcc, s51, v140
	s_nop 0
	v_lshl_add_u64 v[18:19], v[140:141], 0, s[22:23]
	v_cvt_pk_bf16_f32 v13, v16, v17
	v_addc_co_u32_e32 v15, vcc, 0, v141, vcc
	global_store_dwordx4 v[14:15], v[10:13], off sc1
	s_nop 1
	v_cvt_pk_bf16_f32 v10, v54, v55
	v_cvt_pk_bf16_f32 v11, v56, v57
	v_cvt_pk_bf16_f32 v12, v50, v51
	v_cvt_pk_bf16_f32 v13, v52, v53
	global_store_dwordx4 v[18:19], v[10:13], off offset:256 sc1
	v_cvt_pk_bf16_f32 v6, v6, v7
	v_cvt_pk_bf16_f32 v7, v8, v9
	v_cvt_pk_bf16_f32 v8, v2, v3
	v_add_co_u32_e32 v2, vcc, s52, v140
	s_nop 0
	v_lshl_add_u64 v[10:11], v[140:141], 0, s[24:25]
	v_addc_co_u32_e32 v3, vcc, 0, v141, vcc
	s_and_b64 vcc, exec, s[2:3]
	s_mov_b64 s[2:3], -1
	v_cvt_pk_bf16_f32 v9, v4, v5
	global_store_dwordx4 v[2:3], v[6:9], off sc1
	v_cvt_pk_bf16_f32 v2, v34, v35
	v_cvt_pk_bf16_f32 v3, v36, v37
	v_cvt_pk_bf16_f32 v4, v26, v27
	v_cvt_pk_bf16_f32 v5, v28, v29
	global_store_dwordx4 v[10:11], v[2:5], off offset:256 sc1
	s_cbranch_vccnz .LBB0_1487
	s_andn2_b64 vcc, exec, s[0:1]
	s_cbranch_vccnz .LBB0_1486
	s_barrier
	s_branch .LBB0_1486

.LBB0_1871:
	v_lshl_add_u32 v144, s49, 8, v149
	v_ashrrev_i32_e32 v145, 31, v144
	v_lshlrev_b64 v[150:151], 12, v[144:145]
	v_mul_f32_e32 v138, 0xbfb8aa3b, v126
	v_mul_f32_e32 v145, 0xbfb8aa3b, v127
	v_mul_f32_e32 v122, v126, v122
	v_mul_f32_e32 v123, v127, v123
	v_mul_f32_e32 v126, 0xbfb8aa3b, v128
	v_mul_f32_e32 v127, 0xbfb8aa3b, v129
	v_exp_f32_e32 v126, v126
	v_exp_f32_e32 v127, v127
	v_mul_f32_e32 v124, v128, v124
	v_mul_f32_e32 v128, 0xbfb8aa3b, v118
	v_add_f32_e32 v126, 1.0, v126
	v_add_f32_e32 v127, 1.0, v127
	v_rcp_f32_e32 v126, v126
	v_rcp_f32_e32 v127, v127
	v_exp_f32_e32 v128, v128
	v_mul_f32_e32 v125, v129, v125
	v_mul_f32_e32 v124, v126, v124
	v_mul_f32_e32 v125, v127, v125
	v_add_f32_e32 v126, 1.0, v128
	v_mul_f32_e32 v127, 0xbfb8aa3b, v119
	v_rcp_f32_e32 v126, v126
	v_exp_f32_e32 v127, v127
	v_mul_f32_e32 v114, v118, v114
	v_mul_f32_e32 v118, 0xbfb8aa3b, v120
	v_mul_f32_e32 v126, v126, v114
	v_mul_f32_e32 v114, v119, v115
	v_add_f32_e32 v115, 1.0, v127
	v_rcp_f32_e32 v115, v115
	v_exp_f32_e32 v118, v118
	v_mul_f32_e32 v119, 0xbfb8aa3b, v121
	v_exp_f32_e32 v119, v119
	v_exp_f32_e32 v138, v138
	v_exp_f32_e32 v145, v145
	v_mul_f32_e32 v127, v115, v114
	v_add_f32_e32 v114, 1.0, v118
	v_rcp_f32_e32 v114, v114
	v_add_f32_e32 v115, 1.0, v119
	v_add_f32_e32 v138, 1.0, v138
	v_add_f32_e32 v145, 1.0, v145
	v_rcp_f32_e32 v115, v115
	v_rcp_f32_e32 v138, v138
	v_rcp_f32_e32 v145, v145
	v_lshl_or_b32 v146, s50, 7, v157
	v_mul_f32_e32 v116, v120, v116
	v_ashrrev_i32_e32 v147, 31, v146
	v_mul_f32_e32 v128, v114, v116
	v_mul_f32_e32 v114, v121, v117
	v_lshl_add_u64 v[150:151], s[12:13], 0, v[150:151]
	v_mul_f32_e32 v121, v115, v114
	v_lshlrev_b64 v[116:117], 1, v[146:147]
	v_mul_f32_e32 v122, v138, v122
	v_mul_f32_e32 v123, v145, v123
	v_lshl_add_u64 v[114:115], v[150:151], 0, v[116:117]
	v_cvt_pk_bf16_f32 v118, v122, v123
	v_cvt_pk_bf16_f32 v119, v124, v125
	v_cvt_pk_bf16_f32 v120, v126, v127
	v_cvt_pk_bf16_f32 v121, v128, v121
	global_store_dwordx4 v[114:115], v[118:121], off sc1
	v_mul_f32_e32 v106, v110, v106
	v_mul_f32_e32 v107, v111, v107
	v_mul_f32_e32 v120, 0xbfb8aa3b, v110
	v_mul_f32_e32 v121, 0xbfb8aa3b, v111
	v_mul_f32_e32 v110, 0xbfb8aa3b, v112
	v_mul_f32_e32 v111, 0xbfb8aa3b, v113
	v_exp_f32_e32 v110, v110
	v_exp_f32_e32 v111, v111
	v_mul_f32_e32 v108, v112, v108
	v_mul_f32_e32 v112, 0xbfb8aa3b, v102
	v_add_f32_e32 v110, 1.0, v110
	v_add_f32_e32 v111, 1.0, v111
	v_rcp_f32_e32 v110, v110
	v_rcp_f32_e32 v111, v111
	v_exp_f32_e32 v112, v112
	v_mul_f32_e32 v109, v113, v109
	v_mul_f32_e32 v108, v110, v108
	v_mul_f32_e32 v109, v111, v109
	v_add_f32_e32 v110, 1.0, v112
	v_mul_f32_e32 v111, 0xbfb8aa3b, v103
	v_rcp_f32_e32 v110, v110
	v_exp_f32_e32 v111, v111
	v_mul_f32_e32 v98, v102, v98
	v_mul_f32_e32 v102, 0xbfb8aa3b, v104
	v_mul_f32_e32 v110, v110, v98
	v_mul_f32_e32 v98, v103, v99
	v_add_f32_e32 v99, 1.0, v111
	v_rcp_f32_e32 v99, v99
	v_exp_f32_e32 v102, v102
	v_mul_f32_e32 v103, 0xbfb8aa3b, v105
	v_exp_f32_e32 v103, v103
	v_exp_f32_e32 v120, v120
	v_exp_f32_e32 v121, v121
	v_mul_f32_e32 v111, v99, v98
	v_add_f32_e32 v98, 1.0, v102
	v_rcp_f32_e32 v98, v98
	v_add_f32_e32 v99, 1.0, v103
	v_add_f32_e32 v120, 1.0, v120
	v_add_f32_e32 v121, 1.0, v121
	v_rcp_f32_e32 v99, v99
	v_or_b32_e32 v118, 16, v144
	v_rcp_f32_e32 v120, v120
	v_rcp_f32_e32 v121, v121
	v_ashrrev_i32_e32 v119, 31, v118
	v_mul_f32_e32 v100, v104, v100
	v_lshlrev_b64 v[118:119], 12, v[118:119]
	v_mul_f32_e32 v104, v98, v100
	v_mul_f32_e32 v98, v105, v101
	v_lshl_add_u64 v[118:119], s[12:13], 0, v[118:119]
	v_mul_f32_e32 v101, v99, v98
	v_mul_f32_e32 v106, v120, v106
	v_mul_f32_e32 v107, v121, v107
	v_lshl_add_u64 v[102:103], v[118:119], 0, v[116:117]
	v_cvt_pk_bf16_f32 v98, v106, v107
	v_cvt_pk_bf16_f32 v99, v108, v109
	v_cvt_pk_bf16_f32 v100, v110, v111
	v_cvt_pk_bf16_f32 v101, v104, v101
	global_store_dwordx4 v[102:103], v[98:101], off sc1
	v_mul_f32_e32 v90, v94, v90
	v_mul_f32_e32 v91, v95, v91
	v_mul_f32_e32 v100, 0xbfb8aa3b, v94
	v_mul_f32_e32 v101, 0xbfb8aa3b, v95
	v_mul_f32_e32 v94, 0xbfb8aa3b, v96
	v_mul_f32_e32 v95, 0xbfb8aa3b, v97
	v_exp_f32_e32 v94, v94
	v_exp_f32_e32 v95, v95
	v_mul_f32_e32 v92, v96, v92
	v_mul_f32_e32 v96, 0xbfb8aa3b, v86
	v_add_f32_e32 v94, 1.0, v94
	v_add_f32_e32 v95, 1.0, v95
	v_rcp_f32_e32 v94, v94
	v_rcp_f32_e32 v95, v95
	v_exp_f32_e32 v96, v96
	v_mul_f32_e32 v93, v97, v93
	v_mul_f32_e32 v92, v94, v92
	v_mul_f32_e32 v93, v95, v93
	v_add_f32_e32 v94, 1.0, v96
	v_mul_f32_e32 v95, 0xbfb8aa3b, v87
	v_rcp_f32_e32 v94, v94
	v_exp_f32_e32 v95, v95
	v_mul_f32_e32 v82, v86, v82
	v_mul_f32_e32 v86, 0xbfb8aa3b, v88
	v_mul_f32_e32 v94, v94, v82
	v_mul_f32_e32 v82, v87, v83
	v_add_f32_e32 v83, 1.0, v95
	v_rcp_f32_e32 v83, v83
	v_exp_f32_e32 v86, v86
	v_mul_f32_e32 v87, 0xbfb8aa3b, v89
	v_exp_f32_e32 v87, v87
	v_exp_f32_e32 v100, v100
	v_exp_f32_e32 v101, v101
	v_mul_f32_e32 v95, v83, v82
	v_add_f32_e32 v82, 1.0, v86
	v_rcp_f32_e32 v82, v82
	v_add_f32_e32 v83, 1.0, v87
	v_add_f32_e32 v100, 1.0, v100
	v_add_f32_e32 v101, 1.0, v101
	v_rcp_f32_e32 v83, v83
	v_or_b32_e32 v98, 32, v144
	v_rcp_f32_e32 v100, v100
	v_rcp_f32_e32 v101, v101
	v_ashrrev_i32_e32 v99, 31, v98
	v_mul_f32_e32 v84, v88, v84
	v_lshlrev_b64 v[98:99], 12, v[98:99]
	v_mul_f32_e32 v88, v82, v84
	v_mul_f32_e32 v82, v89, v85
	v_lshl_add_u64 v[98:99], s[12:13], 0, v[98:99]
	v_mul_f32_e32 v85, v83, v82
	v_mul_f32_e32 v90, v100, v90
	v_mul_f32_e32 v91, v101, v91
	v_lshl_add_u64 v[86:87], v[98:99], 0, v[116:117]
	v_cvt_pk_bf16_f32 v82, v90, v91
	v_cvt_pk_bf16_f32 v83, v92, v93
	v_cvt_pk_bf16_f32 v84, v94, v95
	v_cvt_pk_bf16_f32 v85, v88, v85
	global_store_dwordx4 v[86:87], v[82:85], off sc1
	v_mul_f32_e32 v74, v78, v74
	v_mul_f32_e32 v75, v79, v75
	v_mul_f32_e32 v84, 0xbfb8aa3b, v78
	v_mul_f32_e32 v85, 0xbfb8aa3b, v79
	v_mul_f32_e32 v78, 0xbfb8aa3b, v80
	v_mul_f32_e32 v79, 0xbfb8aa3b, v81
	v_exp_f32_e32 v78, v78
	v_exp_f32_e32 v79, v79
	v_mul_f32_e32 v76, v80, v76
	v_mul_f32_e32 v80, 0xbfb8aa3b, v70
	v_add_f32_e32 v78, 1.0, v78
	v_add_f32_e32 v79, 1.0, v79
	v_rcp_f32_e32 v78, v78
	v_rcp_f32_e32 v79, v79
	v_exp_f32_e32 v80, v80
	v_mul_f32_e32 v77, v81, v77
	v_mul_f32_e32 v76, v78, v76
	v_mul_f32_e32 v77, v79, v77
	v_add_f32_e32 v78, 1.0, v80
	v_mul_f32_e32 v79, 0xbfb8aa3b, v71
	v_rcp_f32_e32 v78, v78
	v_exp_f32_e32 v79, v79
	v_mul_f32_e32 v66, v70, v66
	v_mul_f32_e32 v70, 0xbfb8aa3b, v72
	v_mul_f32_e32 v78, v78, v66
	v_mul_f32_e32 v66, v71, v67
	v_add_f32_e32 v67, 1.0, v79
	v_rcp_f32_e32 v67, v67
	v_exp_f32_e32 v70, v70
	v_mul_f32_e32 v71, 0xbfb8aa3b, v73
	v_exp_f32_e32 v71, v71
	v_exp_f32_e32 v84, v84
	v_exp_f32_e32 v85, v85
	v_mul_f32_e32 v79, v67, v66
	v_add_f32_e32 v66, 1.0, v70
	v_rcp_f32_e32 v66, v66
	v_add_f32_e32 v67, 1.0, v71
	v_add_f32_e32 v84, 1.0, v84
	v_add_f32_e32 v85, 1.0, v85
	v_rcp_f32_e32 v67, v67
	v_rcp_f32_e32 v84, v84
	v_rcp_f32_e32 v85, v85
	v_mul_f32_e32 v68, v72, v68
	v_mul_f32_e32 v72, v66, v68
	v_mul_f32_e32 v66, v73, v69
	v_mul_f32_e32 v69, v67, v66
	v_mul_f32_e32 v74, v84, v74
	v_mul_f32_e32 v75, v85, v75
	v_cvt_pk_bf16_f32 v66, v74, v75
	v_cvt_pk_bf16_f32 v67, v76, v77
	v_cvt_pk_bf16_f32 v68, v78, v79
	v_cvt_pk_bf16_f32 v69, v72, v69
	v_mul_f32_e32 v72, 0xbfb8aa3b, v62
	v_mul_f32_e32 v73, 0xbfb8aa3b, v63
	v_mul_f32_e32 v58, v58, v62
	v_mul_f32_e32 v59, v59, v63
	v_mul_f32_e32 v62, 0xbfb8aa3b, v64
	v_mul_f32_e32 v63, 0xbfb8aa3b, v65
	v_exp_f32_e32 v62, v62
	v_exp_f32_e32 v63, v63
	v_mul_f32_e32 v60, v60, v64
	v_mul_f32_e32 v64, 0xbfb8aa3b, v54
	v_add_f32_e32 v62, 1.0, v62
	v_add_f32_e32 v63, 1.0, v63
	v_rcp_f32_e32 v62, v62
	v_rcp_f32_e32 v63, v63
	v_exp_f32_e32 v64, v64
	v_mul_f32_e32 v61, v61, v65
	v_mul_f32_e32 v60, v60, v62
	v_mul_f32_e32 v61, v61, v63
	v_add_f32_e32 v62, 1.0, v64
	v_mul_f32_e32 v63, 0xbfb8aa3b, v55
	v_rcp_f32_e32 v62, v62
	v_exp_f32_e32 v63, v63
	v_mul_f32_e32 v50, v50, v54
	v_mul_f32_e32 v52, v52, v56
	v_mul_f32_e32 v54, v50, v62
	v_mul_f32_e32 v50, v51, v55
	v_add_f32_e32 v51, 1.0, v63
	v_mul_f32_e32 v55, 0xbfb8aa3b, v56
	v_rcp_f32_e32 v51, v51
	v_exp_f32_e32 v55, v55
	v_mul_f32_e32 v62, 0xbfb8aa3b, v57
	v_mul_f32_e32 v56, 0xbfb8aa3b, v46
	v_mul_f32_e32 v63, v50, v51
	v_add_f32_e32 v50, 1.0, v55
	v_rcp_f32_e32 v50, v50
	v_mul_f32_e32 v34, v34, v46
	v_mul_f32_e32 v35, v35, v47
	v_mul_f32_e32 v46, 0xbfb8aa3b, v48
	v_mul_f32_e32 v55, v52, v50
	v_mul_f32_e32 v50, v53, v57
	v_mul_f32_e32 v57, 0xbfb8aa3b, v47
	v_mul_f32_e32 v47, 0xbfb8aa3b, v49
	v_exp_f32_e32 v46, v46
	v_exp_f32_e32 v47, v47
	v_mul_f32_e32 v36, v36, v48
	v_mul_f32_e32 v48, 0xbfb8aa3b, v30
	v_add_f32_e32 v46, 1.0, v46
	v_add_f32_e32 v47, 1.0, v47
	v_rcp_f32_e32 v46, v46
	v_rcp_f32_e32 v47, v47
	v_exp_f32_e32 v48, v48
	v_mul_f32_e32 v37, v37, v49
	v_mul_f32_e32 v36, v36, v46
	v_mul_f32_e32 v37, v37, v47
	v_add_f32_e32 v46, 1.0, v48
	v_mul_f32_e32 v47, 0xbfb8aa3b, v31
	v_or_b32_e32 v82, 48, v144
	v_rcp_f32_e32 v46, v46
	v_exp_f32_e32 v47, v47
	v_ashrrev_i32_e32 v83, 31, v82
	v_exp_f32_e32 v72, v72
	v_exp_f32_e32 v73, v73
	v_exp_f32_e32 v62, v62
	v_lshlrev_b64 v[82:83], 12, v[82:83]
	v_lshl_add_u64 v[82:83], s[12:13], 0, v[82:83]
	v_mul_f32_e32 v26, v26, v30
	v_lshl_add_u64 v[70:71], v[82:83], 0, v[116:117]
	v_mul_f32_e32 v30, v26, v46
	v_mul_f32_e32 v26, v27, v31
	v_add_f32_e32 v27, 1.0, v47
	v_mul_f32_e32 v31, 0xbfb8aa3b, v32
	global_store_dwordx4 v[70:71], v[66:69], off sc1
	v_add_f32_e32 v51, 1.0, v62
	v_rcp_f32_e32 v27, v27
	v_add_f32_e32 v66, 1.0, v72
	v_add_f32_e32 v67, 1.0, v73
	v_exp_f32_e32 v31, v31
	v_rcp_f32_e32 v66, v66
	v_rcp_f32_e32 v67, v67
	v_rcp_f32_e32 v51, v51
	v_mul_f32_e32 v46, 0xbfb8aa3b, v33
	v_exp_f32_e32 v56, v56
	v_exp_f32_e32 v57, v57
	v_exp_f32_e32 v46, v46
	v_mul_f32_e32 v47, v26, v27
	v_add_f32_e32 v26, 1.0, v31
	v_mul_f32_e32 v58, v58, v66
	v_mul_f32_e32 v59, v59, v67
	v_mul_f32_e32 v53, v50, v51
	v_cvt_pk_bf16_f32 v50, v58, v59
	v_cvt_pk_bf16_f32 v51, v60, v61
	v_cvt_pk_bf16_f32 v52, v54, v63
	v_add_co_u32_e32 v54, vcc, s45, v114
	v_rcp_f32_e32 v26, v26
	v_cvt_pk_bf16_f32 v53, v55, v53
	s_nop 0
	v_addc_co_u32_e32 v55, vcc, 0, v115, vcc
	global_store_dwordx4 v[54:55], v[50:53], off sc1
	v_add_f32_e32 v27, 1.0, v46
	v_rcp_f32_e32 v27, v27
	v_add_f32_e32 v50, 1.0, v56
	v_add_f32_e32 v51, 1.0, v57
	v_rcp_f32_e32 v50, v50
	v_rcp_f32_e32 v51, v51
	v_mul_f32_e32 v28, v28, v32
	v_mul_f32_e32 v31, v28, v26
	v_mul_f32_e32 v26, v29, v33
	v_mul_f32_e32 v32, 0xbfb8aa3b, v18
	v_mul_f32_e32 v33, 0xbfb8aa3b, v19
	v_exp_f32_e32 v32, v32
	v_exp_f32_e32 v33, v33
	v_mul_f32_e32 v34, v34, v50
	v_mul_f32_e32 v35, v35, v51
	v_mul_f32_e32 v29, v26, v27
	v_cvt_pk_bf16_f32 v26, v34, v35
	v_cvt_pk_bf16_f32 v27, v36, v37
	v_cvt_pk_bf16_f32 v28, v30, v47
	v_add_co_u32_e32 v30, vcc, s46, v114
	v_cvt_pk_bf16_f32 v29, v31, v29
	v_mul_f32_e32 v18, v18, v42
	s_nop 0
	v_addc_co_u32_e32 v31, vcc, 0, v115, vcc
	global_store_dwordx4 v[30:31], v[26:29], off sc1
	v_mul_f32_e32 v19, v19, v43
	s_mov_b64 s[0:1], -1
	v_add_f32_e32 v26, 1.0, v32
	v_add_f32_e32 v27, 1.0, v33
	v_rcp_f32_e32 v26, v26
	v_rcp_f32_e32 v27, v27
	v_mul_f32_e32 v28, 0xbfb8aa3b, v10
	v_exp_f32_e32 v28, v28
	v_mul_f32_e32 v18, v26, v18
	v_mul_f32_e32 v19, v27, v19
	v_mul_f32_e32 v26, 0xbfb8aa3b, v20
	v_mul_f32_e32 v27, 0xbfb8aa3b, v21
	v_exp_f32_e32 v26, v26
	v_exp_f32_e32 v27, v27
	v_mul_f32_e32 v20, v20, v44
	v_mul_f32_e32 v21, v21, v45
	v_add_f32_e32 v26, 1.0, v26
	v_add_f32_e32 v27, 1.0, v27
	v_rcp_f32_e32 v26, v26
	v_rcp_f32_e32 v27, v27
	v_mul_f32_e32 v10, v10, v38
	v_mul_f32_e32 v20, v26, v20
	v_mul_f32_e32 v21, v27, v21
	v_add_f32_e32 v26, 1.0, v28
	v_mul_f32_e32 v27, 0xbfb8aa3b, v11
	v_rcp_f32_e32 v26, v26
	v_exp_f32_e32 v27, v27
	v_mul_f32_e32 v28, 0xbfb8aa3b, v13
	v_exp_f32_e32 v28, v28
	v_mul_f32_e32 v26, v26, v10
	v_mul_f32_e32 v10, v11, v39
	v_add_f32_e32 v11, 1.0, v27
	v_mul_f32_e32 v27, 0xbfb8aa3b, v12
	v_rcp_f32_e32 v11, v11
	v_exp_f32_e32 v27, v27
	v_mul_f32_e32 v12, v12, v40
	v_mul_f32_e32 v29, v11, v10
	v_add_f32_e32 v10, 1.0, v27
	v_rcp_f32_e32 v10, v10
	v_add_f32_e32 v11, 1.0, v28
	v_rcp_f32_e32 v11, v11
	v_mul_f32_e32 v27, v10, v12
	v_mul_f32_e32 v10, v13, v41
	v_mul_f32_e32 v13, v11, v10
	v_cvt_pk_bf16_f32 v10, v18, v19
	v_cvt_pk_bf16_f32 v11, v20, v21
	v_mul_f32_e32 v20, 0xbfb8aa3b, v6
	v_mul_f32_e32 v21, 0xbfb8aa3b, v7
	v_exp_f32_e32 v20, v20
	v_exp_f32_e32 v21, v21
	v_add_co_u32_e32 v18, vcc, s47, v114
	v_cvt_pk_bf16_f32 v12, v26, v29
	v_cvt_pk_bf16_f32 v13, v27, v13
	v_mul_f32_e32 v6, v6, v22
	s_nop 0
	v_addc_co_u32_e32 v19, vcc, 0, v115, vcc
	global_store_dwordx4 v[18:19], v[10:13], off sc1
	v_mul_f32_e32 v7, v7, v23
	s_nop 0
	v_add_f32_e32 v10, 1.0, v20
	v_add_f32_e32 v11, 1.0, v21
	v_rcp_f32_e32 v10, v10
	v_rcp_f32_e32 v11, v11
	v_mul_f32_e32 v12, 0xbfb8aa3b, v2
	v_exp_f32_e32 v12, v12
	v_mul_f32_e32 v6, v10, v6
	v_mul_f32_e32 v7, v11, v7
	v_mul_f32_e32 v10, 0xbfb8aa3b, v8
	v_mul_f32_e32 v11, 0xbfb8aa3b, v9
	v_exp_f32_e32 v10, v10
	v_exp_f32_e32 v11, v11
	v_mul_f32_e32 v8, v8, v24
	v_mul_f32_e32 v9, v9, v25
	v_add_f32_e32 v10, 1.0, v10
	v_add_f32_e32 v11, 1.0, v11
	v_rcp_f32_e32 v10, v10
	v_rcp_f32_e32 v11, v11
	v_mul_f32_e32 v2, v2, v14
	v_mul_f32_e32 v8, v10, v8
	v_mul_f32_e32 v9, v11, v9
	v_add_f32_e32 v10, 1.0, v12
	v_mul_f32_e32 v11, 0xbfb8aa3b, v3
	v_rcp_f32_e32 v10, v10
	v_exp_f32_e32 v11, v11
	v_mul_f32_e32 v12, 0xbfb8aa3b, v5
	v_exp_f32_e32 v12, v12
	v_mul_f32_e32 v10, v10, v2
	v_mul_f32_e32 v2, v3, v15
	v_add_f32_e32 v3, 1.0, v11
	v_mul_f32_e32 v11, 0xbfb8aa3b, v4
	v_rcp_f32_e32 v3, v3
	v_exp_f32_e32 v11, v11
	v_mul_f32_e32 v4, v4, v16
	v_mul_f32_e32 v13, v3, v2
	v_add_f32_e32 v2, 1.0, v11
	v_rcp_f32_e32 v2, v2
	v_add_f32_e32 v3, 1.0, v12
	v_rcp_f32_e32 v3, v3
	v_mul_f32_e32 v11, v2, v4
	v_mul_f32_e32 v2, v5, v17
	v_mul_f32_e32 v5, v3, v2
	v_cvt_pk_bf16_f32 v2, v6, v7
	v_add_co_u32_e32 v6, vcc, 0xb0000, v114
	v_cvt_pk_bf16_f32 v3, v8, v9
	v_cvt_pk_bf16_f32 v4, v10, v13
	v_cvt_pk_bf16_f32 v5, v11, v5
	s_nop 1
	v_addc_co_u32_e32 v7, vcc, 0, v115, vcc
	s_and_b64 vcc, exec, s[2:3]
	global_store_dwordx4 v[6:7], v[2:5], off sc1
	s_cbranch_vccnz .LBB0_1858
	s_andn2_b64 vcc, exec, s[10:11]
	s_cbranch_vccnz .LBB0_1857
	s_barrier
	s_branch .LBB0_1857

.LBB0_1948:
	v_lshl_add_u32 v142, s56, 8, v151
	v_lshl_or_b32 v140, s57, 8, v153
	v_ashrrev_i32_e32 v143, 31, v142
	v_ashrrev_i32_e32 v141, 31, v140
	v_lshlrev_b64 v[144:145], 12, v[142:143]
	v_lshl_add_u64 v[144:145], s[10:11], 0, v[144:145]
	v_lshlrev_b64 v[146:147], 1, v[140:141]
	v_lshl_add_u64 v[140:141], v[144:145], 0, v[146:147]
	v_cvt_pk_bf16_f32 v126, v126, v127
	v_cvt_pk_bf16_f32 v127, v128, v129
	v_cvt_pk_bf16_f32 v128, v122, v123
	v_cvt_pk_bf16_f32 v129, v124, v125
	global_store_dwordx4 v[140:141], v[126:129], off sc1
	v_cvt_pk_bf16_f32 v114, v114, v115
	v_cvt_pk_bf16_f32 v115, v116, v117
	v_cvt_pk_bf16_f32 v116, v106, v107
	v_or_b32_e32 v106, 16, v142
	v_ashrrev_i32_e32 v107, 31, v106
	v_lshlrev_b64 v[106:107], 12, v[106:107]
	v_lshl_add_u64 v[106:107], s[10:11], 0, v[106:107]
	v_cvt_pk_bf16_f32 v117, v108, v109
	global_store_dwordx4 v[140:141], v[114:117], off offset:256 sc1
	s_nop 1
	v_lshl_add_u64 v[114:115], v[106:107], 0, v[146:147]
	v_cvt_pk_bf16_f32 v106, v118, v119
	v_cvt_pk_bf16_f32 v107, v120, v121
	v_cvt_pk_bf16_f32 v108, v110, v111
	v_cvt_pk_bf16_f32 v109, v112, v113
	global_store_dwordx4 v[114:115], v[106:109], off sc1
	v_cvt_pk_bf16_f32 v98, v98, v99
	v_cvt_pk_bf16_f32 v99, v100, v101
	v_cvt_pk_bf16_f32 v100, v90, v91
	v_or_b32_e32 v90, 32, v142
	v_ashrrev_i32_e32 v91, 31, v90
	v_lshlrev_b64 v[90:91], 12, v[90:91]
	v_lshl_add_u64 v[90:91], s[10:11], 0, v[90:91]
	v_cvt_pk_bf16_f32 v101, v92, v93
	global_store_dwordx4 v[114:115], v[98:101], off offset:256 sc1
	s_nop 1
	v_lshl_add_u64 v[98:99], v[90:91], 0, v[146:147]
	v_cvt_pk_bf16_f32 v90, v102, v103
	v_cvt_pk_bf16_f32 v91, v104, v105
	v_cvt_pk_bf16_f32 v92, v94, v95
	v_cvt_pk_bf16_f32 v93, v96, v97
	global_store_dwordx4 v[98:99], v[90:93], off sc1
	v_cvt_pk_bf16_f32 v82, v82, v83
	v_cvt_pk_bf16_f32 v83, v84, v85
	v_cvt_pk_bf16_f32 v84, v74, v75
	v_or_b32_e32 v74, 48, v142
	v_ashrrev_i32_e32 v75, 31, v74
	v_lshlrev_b64 v[74:75], 12, v[74:75]
	v_lshl_add_u64 v[74:75], s[10:11], 0, v[74:75]
	v_cvt_pk_bf16_f32 v85, v76, v77
	global_store_dwordx4 v[98:99], v[82:85], off offset:256 sc1
	s_nop 1
	v_lshl_add_u64 v[82:83], v[74:75], 0, v[146:147]
	v_cvt_pk_bf16_f32 v74, v86, v87
	v_cvt_pk_bf16_f32 v75, v88, v89
	v_cvt_pk_bf16_f32 v76, v78, v79
	v_cvt_pk_bf16_f32 v77, v80, v81
	global_store_dwordx4 v[82:83], v[74:77], off sc1
	v_cvt_pk_bf16_f32 v70, v70, v71
	v_cvt_pk_bf16_f32 v71, v72, v73
	v_cvt_pk_bf16_f32 v72, v66, v67
	v_cvt_pk_bf16_f32 v73, v68, v69
	global_store_dwordx4 v[82:83], v[70:73], off offset:256 sc1
	v_cvt_pk_bf16_f32 v62, v62, v63
	v_cvt_pk_bf16_f32 v63, v64, v65
	v_cvt_pk_bf16_f32 v64, v58, v59
	v_add_co_u32_e32 v58, vcc, s46, v140
	v_lshl_add_u64 v[66:67], v[140:141], 0, s[18:19]
	s_nop 0
	v_addc_co_u32_e32 v59, vcc, 0, v141, vcc
	v_cvt_pk_bf16_f32 v65, v60, v61
	global_store_dwordx4 v[58:59], v[62:65], off sc1
	v_cvt_pk_bf16_f32 v42, v42, v43
	v_cvt_pk_bf16_f32 v43, v44, v45
	v_cvt_pk_bf16_f32 v44, v30, v31
	v_cvt_pk_bf16_f32 v45, v32, v33
	global_store_dwordx4 v[66:67], v[42:45], off offset:256 sc1
	v_cvt_pk_bf16_f32 v30, v46, v47
	v_cvt_pk_bf16_f32 v31, v48, v49
	v_cvt_pk_bf16_f32 v32, v38, v39
	v_add_co_u32_e32 v38, vcc, s52, v140
	s_nop 0
	v_lshl_add_u64 v[42:43], v[140:141], 0, s[20:21]
	v_addc_co_u32_e32 v39, vcc, 0, v141, vcc
	v_cvt_pk_bf16_f32 v33, v40, v41
	global_store_dwordx4 v[38:39], v[30:33], off sc1
	v_cvt_pk_bf16_f32 v18, v18, v19
	v_cvt_pk_bf16_f32 v19, v20, v21
	v_cvt_pk_bf16_f32 v20, v10, v11
	v_cvt_pk_bf16_f32 v21, v12, v13
	global_store_dwordx4 v[42:43], v[18:21], off offset:256 sc1
	v_cvt_pk_bf16_f32 v10, v22, v23
	v_cvt_pk_bf16_f32 v11, v24, v25
	v_cvt_pk_bf16_f32 v12, v14, v15
	v_add_co_u32_e32 v14, vcc, s53, v140
	s_nop 0
	v_lshl_add_u64 v[18:19], v[140:141], 0, s[22:23]
	v_cvt_pk_bf16_f32 v13, v16, v17
	v_addc_co_u32_e32 v15, vcc, 0, v141, vcc
	global_store_dwordx4 v[14:15], v[10:13], off sc1
	s_nop 1
	v_cvt_pk_bf16_f32 v10, v54, v55
	v_cvt_pk_bf16_f32 v11, v56, v57
	v_cvt_pk_bf16_f32 v12, v50, v51
	v_cvt_pk_bf16_f32 v13, v52, v53
	global_store_dwordx4 v[18:19], v[10:13], off offset:256 sc1
	v_cvt_pk_bf16_f32 v6, v6, v7
	v_cvt_pk_bf16_f32 v7, v8, v9
	v_cvt_pk_bf16_f32 v8, v2, v3
	v_add_co_u32_e32 v2, vcc, s54, v140
	s_nop 0
	v_lshl_add_u64 v[10:11], v[140:141], 0, s[24:25]
	v_addc_co_u32_e32 v3, vcc, 0, v141, vcc
	s_and_b64 vcc, exec, s[2:3]
	s_mov_b64 s[2:3], -1
	v_cvt_pk_bf16_f32 v9, v4, v5
	global_store_dwordx4 v[2:3], v[6:9], off sc1
	v_cvt_pk_bf16_f32 v2, v34, v35
	v_cvt_pk_bf16_f32 v3, v36, v37
	v_cvt_pk_bf16_f32 v4, v26, v27
	v_cvt_pk_bf16_f32 v5, v28, v29
	global_store_dwordx4 v[10:11], v[2:5], off offset:256 sc1
	s_cbranch_vccnz .LBB0_1935
	s_andn2_b64 vcc, exec, s[0:1]
	s_cbranch_vccnz .LBB0_1934
	s_barrier
	s_branch .LBB0_1934
